# MoE K-loops: four wave groups (wave&3) each run the weight-tile block at a different point of the K-tile interval (first / after first fragment reads / between k-steps / last)
# baseline (speedup 1.0000x reference)
.LBB0_1013:
	s_or_b64 exec, exec, s[34:35]
	s_lshl_b64 s[34:35], s[10:11], 22
	s_add_u32 s10, s12, s34
	s_addc_u32 s52, s13, s35
	s_lshl_b32 s34, s36, 9
	s_lshl_b32 s35, s46, 6
	s_sub_i32 s34, s35, s34
	s_ashr_i32 s35, s34, 31
	s_lshl_b64 s[36:37], s[34:35], 2
	s_add_u32 s36, s10, s36
	s_addc_u32 s37, s52, s37
	v_or_b32_e32 v146, v3, v1
	s_waitcnt lgkmcnt(0)
	v_readfirstlane_b32 s51, v2
	v_lshl_add_u64 v[2:3], s[36:37], 0, v[152:153]
	v_lshl_add_u64 v[156:157], v[2:3], 0, v[148:149]
	s_mov_b64 s[36:37], -1
	s_cmp_ge_i32 s38, s50
	v_lshl_add_u64 v[132:133], v[156:157], 0, s[22:23]
	v_lshl_add_u64 v[130:131], v[156:157], 0, s[24:25]
	v_lshl_add_u64 v[134:135], v[156:157], 0, s[26:27]
	v_lshl_add_u64 v[138:139], v[156:157], 0, s[28:29]
	v_lshl_add_u64 v[142:143], v[156:157], 0, s[30:31]
	s_cbranch_scc0 .LBB0_1017
	global_load_dwordx4 v[2:5], v[156:157], off sc1 nt
	s_mov_b32 m0, s39
	global_load_dwordx4 v[6:9], v[132:133], off sc1 nt
	v_lshl_add_u64 v[50:51], s[14:15], 0, v[146:147]
	global_load_lds_dwordx4 v146, s[14:15]
	global_load_dwordx4 v[34:37], v[130:131], off sc1 nt
	global_load_dwordx4 v[38:41], v[134:135], off sc1 nt
	s_mov_b32 m0, s40
	s_nop 0
	global_load_lds_dwordx4 v146, s[16:17]
	s_waitcnt vmcnt(4)
	s_nop 0
	v_cvt_pk_bf16_f32 v2, v2, v6
	ds_write_b32 v169, v2 offset:49152
	v_cvt_pk_bf16_f32 v2, v3, v7
	ds_write_b32 v169, v2 offset:49216
	v_cvt_pk_bf16_f32 v2, v4, v8
	ds_write_b32 v169, v2 offset:49280
	v_cvt_pk_bf16_f32 v2, v5, v9
	ds_write_b32 v169, v2 offset:49344
	global_load_dwordx4 v[42:45], v[138:139], off sc1 nt
	global_load_dwordx4 v[46:49], v[142:143], off sc1 nt
	s_waitcnt vmcnt(5)
	s_mov_b32 m0, s41
	s_waitcnt lgkmcnt(0)
	s_barrier
	global_load_lds_dwordx4 v146, s[18:19]
	v_mov_b32_e32 v2, 0
	s_mov_b32 s37, -2
	s_movk_i32 s36, 0x80
	v_mov_b32_e32 v3, v2
	v_mov_b32_e32 v4, v2
	v_mov_b32_e32 v5, v2
	v_mov_b32_e32 v6, v2
	v_mov_b32_e32 v7, v2
	v_mov_b32_e32 v8, v2
	v_mov_b32_e32 v9, v2
	v_mov_b32_e32 v10, v2
	v_mov_b32_e32 v11, v2
	v_mov_b32_e32 v12, v2
	v_mov_b32_e32 v13, v2
	v_mov_b32_e32 v14, v2
	v_mov_b32_e32 v15, v2
	v_mov_b32_e32 v16, v2
	v_mov_b32_e32 v17, v2
	v_mov_b32_e32 v66, v2
	v_mov_b32_e32 v67, v2
	v_mov_b32_e32 v68, v2
	v_mov_b32_e32 v69, v2
	v_mov_b32_e32 v70, v2
	v_mov_b32_e32 v71, v2
	v_mov_b32_e32 v72, v2
	v_mov_b32_e32 v73, v2
	v_mov_b32_e32 v74, v2
	v_mov_b32_e32 v75, v2
	v_mov_b32_e32 v76, v2
	v_mov_b32_e32 v77, v2
	v_mov_b32_e32 v78, v2
	v_mov_b32_e32 v79, v2
	v_mov_b32_e32 v80, v2
	v_mov_b32_e32 v81, v2
	v_mov_b32_e32 v18, v2
	v_mov_b32_e32 v19, v2
	v_mov_b32_e32 v20, v2
	v_mov_b32_e32 v21, v2
	v_mov_b32_e32 v22, v2
	v_mov_b32_e32 v23, v2
	v_mov_b32_e32 v24, v2
	v_mov_b32_e32 v25, v2
	v_mov_b32_e32 v26, v2
	v_mov_b32_e32 v27, v2
	v_mov_b32_e32 v28, v2
	v_mov_b32_e32 v29, v2
	v_mov_b32_e32 v30, v2
	v_mov_b32_e32 v31, v2
	v_mov_b32_e32 v32, v2
	v_mov_b32_e32 v33, v2
	v_mov_b32_e32 v114, v2
	v_mov_b32_e32 v115, v2
	v_mov_b32_e32 v116, v2
	v_mov_b32_e32 v117, v2
	v_mov_b32_e32 v118, v2
	v_mov_b32_e32 v119, v2
	v_mov_b32_e32 v120, v2
	v_mov_b32_e32 v121, v2
	v_mov_b32_e32 v122, v2
	v_mov_b32_e32 v123, v2
	v_mov_b32_e32 v124, v2
	v_mov_b32_e32 v125, v2
	v_mov_b32_e32 v126, v2
	v_mov_b32_e32 v127, v2
	v_mov_b32_e32 v128, v2
	v_mov_b32_e32 v129, v2
	v_readfirstlane_b32 s98, v250
	s_bfe_u32 s98, s98, 0x20006
	s_cmp_eq_u32 s98, 1
	s_cbranch_scc1 .Lmoe_G1_1015
	s_cmp_eq_u32 s98, 2
	s_cbranch_scc1 .Lmoe_G2_1015
	s_cmp_eq_u32 s98, 3
	s_cbranch_scc1 .Lmoe_G3_1015
.LBB0_1015:
	s_mul_i32 s53, s37, 0xab
	s_add_i32 s10, s53, 0x357
	s_bfe_u32 s10, s10, 0x70009
	s_mul_i32 s10, s10, 3
	s_sub_i32 s10, s37, s10
	s_add_i32 s10, s10, 5
	s_and_b32 s10, s10, 0xff
	s_lshl_b32 s10, s10, 14
	s_add_i32 s56, s39, s10
	s_add_i32 s52, s37, 2
	s_waitcnt vmcnt(4)
	s_sub_i32 s10, s36, 32
	v_cvt_pk_bf16_f32 v34, v34, v38
	s_cmp_lt_u32 s52, 61
	ds_write_b32 v169, v34 offset:57344
	v_cvt_pk_bf16_f32 v34, v35, v39
	s_cselect_b32 s10, s10, 0x7e0
	ds_write_b32 v169, v34 offset:57408
	v_cvt_pk_bf16_f32 v34, v36, v40
	s_lshl_b64 s[54:55], s[10:11], 11
	ds_write_b32 v169, v34 offset:57472
	v_cvt_pk_bf16_f32 v34, v37, v41
	ds_write_b32 v169, v34 offset:57536
	v_lshl_add_u64 v[38:39], v[156:157], 0, s[54:55]
	global_load_dwordx4 v[34:37], v[38:39], off sc1 nt
	v_lshl_add_u64 v[38:39], v[38:39], 0, s[22:23]
	global_load_dwordx4 v[38:41], v[38:39], off sc1 nt
	v_add_u32_e32 v93, s56, v160
	v_add_u32_e32 v52, v93, v163
	v_add_u32_e32 v92, v161, v162
	ds_read_b64 v[64:65], v52
	ds_read_b128 v[52:55], v92 offset:49152
	ds_read_b128 v[56:59], v92 offset:51200
	ds_read_b128 v[60:63], v92 offset:53248
	ds_read_b128 v[82:85], v92 offset:55296
	s_waitcnt lgkmcnt(0)
	v_cvt_pk_f32_fp8_e32 v[86:87], v64
	v_cvt_pk_f32_fp8_sdwa v[88:89], v64 src0_sel:WORD_1
	v_cvt_pk_f32_fp8_e32 v[90:91], v65
	v_cvt_pk_f32_fp8_sdwa v[64:65], v65 src0_sel:WORD_1
	v_cvt_pk_bf16_f32 v86, v86, v87
	v_cvt_pk_bf16_f32 v87, v88, v89
	v_cvt_pk_bf16_f32 v88, v90, v91
	v_cvt_pk_bf16_f32 v89, v64, v65
	s_nop 1
	v_mfma_f32_32x32x16_bf16 v[114:129], v[52:55], v[86:89], v[114:129]
	v_mfma_f32_32x32x16_bf16 v[18:33], v[56:59], v[86:89], v[18:33]
	v_mfma_f32_32x32x16_bf16 v[66:81], v[60:63], v[86:89], v[66:81]
	v_mfma_f32_32x32x16_bf16 v[2:17], v[82:85], v[86:89], v[2:17]
	v_add_u32_e32 v52, v93, v165
	v_add_u32_e32 v94, v161, v164
	ds_read_b64 v[64:65], v52
	ds_read_b128 v[52:55], v94 offset:49152
	ds_read_b128 v[56:59], v94 offset:51200
	ds_read_b128 v[60:63], v94 offset:53248
	ds_read_b128 v[82:85], v94 offset:55296
	s_waitcnt lgkmcnt(0)
	v_cvt_pk_f32_fp8_e32 v[86:87], v64
	v_cvt_pk_f32_fp8_sdwa v[88:89], v64 src0_sel:WORD_1
	v_cvt_pk_f32_fp8_e32 v[90:91], v65
	v_cvt_pk_f32_fp8_sdwa v[64:65], v65 src0_sel:WORD_1
	v_cvt_pk_bf16_f32 v86, v86, v87
	v_cvt_pk_bf16_f32 v87, v88, v89
	v_cvt_pk_bf16_f32 v88, v90, v91
	v_cvt_pk_bf16_f32 v89, v64, v65
	s_nop 0
	v_mfma_f32_32x32x16_bf16 v[114:129], v[52:55], v[86:89], v[114:129]
	v_mfma_f32_32x32x16_bf16 v[18:33], v[56:59], v[86:89], v[18:33]
	v_mfma_f32_32x32x16_bf16 v[66:81], v[60:63], v[86:89], v[66:81]
	v_mfma_f32_32x32x16_bf16 v[2:17], v[82:85], v[86:89], v[2:17]
	s_waitcnt vmcnt(5)
	s_mov_b32 m0, s56
	s_waitcnt lgkmcnt(0)
	s_barrier
	v_lshl_add_u64 v[52:53], v[50:51], 0, s[10:11]
	global_load_lds_dwordx4 v[52:53], off
	s_addk_i32 s53, 0x402
	s_bfe_u32 s10, s53, 0x70009
	s_mul_i32 s10, s10, 3
	s_sub_i32 s10, s37, s10
	s_add_i32 s10, s10, 6
	s_and_b32 s10, s10, 0xff
	s_lshl_b32 s10, s10, 14
	s_add_i32 s37, s39, s10
	s_waitcnt vmcnt(4)
	s_cmp_lt_u32 s52, 60
	v_cvt_pk_bf16_f32 v42, v42, v46
	ds_write_b32 v169, v42 offset:49152
	v_cvt_pk_bf16_f32 v42, v43, v47
	s_cselect_b32 s10, s36, 0x7e0
	ds_write_b32 v169, v42 offset:49216
	v_cvt_pk_bf16_f32 v42, v44, v48
	s_lshl_b64 s[54:55], s[10:11], 11
	ds_write_b32 v169, v42 offset:49280
	v_cvt_pk_bf16_f32 v42, v45, v49
	ds_write_b32 v169, v42 offset:49344
	v_lshl_add_u64 v[46:47], v[156:157], 0, s[54:55]
	global_load_dwordx4 v[42:45], v[46:47], off sc1 nt
	v_lshl_add_u64 v[46:47], v[46:47], 0, s[22:23]
	global_load_dwordx4 v[46:49], v[46:47], off sc1 nt
	v_add_u32_e32 v93, s37, v160
	v_add_u32_e32 v52, v93, v163
	ds_read_b64 v[64:65], v52
	ds_read_b128 v[52:55], v92 offset:57344
	ds_read_b128 v[56:59], v92 offset:59392
	ds_read_b128 v[60:63], v92 offset:61440
	ds_read_b128 v[82:85], v92 offset:63488
	s_waitcnt lgkmcnt(0)
	v_cvt_pk_f32_fp8_e32 v[86:87], v64
	v_cvt_pk_f32_fp8_sdwa v[88:89], v64 src0_sel:WORD_1
	v_cvt_pk_f32_fp8_e32 v[90:91], v65
	v_cvt_pk_f32_fp8_sdwa v[64:65], v65 src0_sel:WORD_1
	v_cvt_pk_bf16_f32 v86, v86, v87
	v_cvt_pk_bf16_f32 v87, v88, v89
	v_cvt_pk_bf16_f32 v88, v90, v91
	v_cvt_pk_bf16_f32 v89, v64, v65
	s_nop 1
	v_mfma_f32_32x32x16_bf16 v[114:129], v[52:55], v[86:89], v[114:129]
	v_mfma_f32_32x32x16_bf16 v[18:33], v[56:59], v[86:89], v[18:33]
	v_mfma_f32_32x32x16_bf16 v[66:81], v[60:63], v[86:89], v[66:81]
	v_mfma_f32_32x32x16_bf16 v[2:17], v[82:85], v[86:89], v[2:17]
	v_add_u32_e32 v52, v93, v165
	ds_read_b64 v[64:65], v52
	ds_read_b128 v[52:55], v94 offset:57344
	ds_read_b128 v[56:59], v94 offset:59392
	ds_read_b128 v[60:63], v94 offset:61440
	ds_read_b128 v[82:85], v94 offset:63488
	s_waitcnt lgkmcnt(0)
	v_cvt_pk_f32_fp8_e32 v[86:87], v64
	v_cvt_pk_f32_fp8_sdwa v[88:89], v64 src0_sel:WORD_1
	v_cvt_pk_f32_fp8_e32 v[90:91], v65
	v_cvt_pk_f32_fp8_sdwa v[64:65], v65 src0_sel:WORD_1
	v_cvt_pk_bf16_f32 v86, v86, v87
	v_cvt_pk_bf16_f32 v87, v88, v89
	v_cvt_pk_bf16_f32 v88, v90, v91
	v_cvt_pk_bf16_f32 v89, v64, v65
	s_nop 0
	v_mfma_f32_32x32x16_bf16 v[114:129], v[52:55], v[86:89], v[114:129]
	v_mfma_f32_32x32x16_bf16 v[18:33], v[56:59], v[86:89], v[18:33]
	v_mfma_f32_32x32x16_bf16 v[66:81], v[60:63], v[86:89], v[66:81]
	v_mfma_f32_32x32x16_bf16 v[2:17], v[82:85], v[86:89], v[2:17]
	s_waitcnt vmcnt(5)
	s_mov_b32 m0, s37
	s_waitcnt lgkmcnt(0)
	s_barrier
	v_lshl_add_u64 v[52:53], v[50:51], 0, s[10:11]
	global_load_lds_dwordx4 v[52:53], off
	s_add_i32 s36, s36, 64
	s_cmp_gt_u32 s52, 61
	s_mov_b32 s37, s52
	s_cbranch_scc0 .LBB0_1015
	s_branch .Lmoe_X_1015

.Lmoe_G2_1015:
	s_mul_i32 s53, s37, 0xab
	s_add_i32 s10, s53, 0x357
	s_bfe_u32 s10, s10, 0x70009
	s_mul_i32 s10, s10, 3
	s_sub_i32 s10, s37, s10
	s_add_i32 s10, s10, 5
	s_and_b32 s10, s10, 0xff
	s_lshl_b32 s10, s10, 14
	s_add_i32 s56, s39, s10
	s_add_i32 s52, s37, 2
	v_add_u32_e32 v93, s56, v160
	v_add_u32_e32 v52, v93, v163
	v_add_u32_e32 v92, v161, v162
	ds_read_b64 v[64:65], v52
	ds_read_b128 v[52:55], v92 offset:49152
	ds_read_b128 v[56:59], v92 offset:51200
	ds_read_b128 v[60:63], v92 offset:53248
	ds_read_b128 v[82:85], v92 offset:55296
	s_waitcnt lgkmcnt(0)
	v_cvt_pk_f32_fp8_e32 v[86:87], v64
	v_cvt_pk_f32_fp8_sdwa v[88:89], v64 src0_sel:WORD_1
	v_cvt_pk_f32_fp8_e32 v[90:91], v65
	v_cvt_pk_f32_fp8_sdwa v[64:65], v65 src0_sel:WORD_1
	v_cvt_pk_bf16_f32 v86, v86, v87
	v_cvt_pk_bf16_f32 v87, v88, v89
	v_cvt_pk_bf16_f32 v88, v90, v91
	v_cvt_pk_bf16_f32 v89, v64, v65
	s_nop 1
	v_mfma_f32_32x32x16_bf16 v[114:129], v[52:55], v[86:89], v[114:129]
	v_mfma_f32_32x32x16_bf16 v[18:33], v[56:59], v[86:89], v[18:33]
	v_mfma_f32_32x32x16_bf16 v[66:81], v[60:63], v[86:89], v[66:81]
	v_mfma_f32_32x32x16_bf16 v[2:17], v[82:85], v[86:89], v[2:17]
	s_waitcnt vmcnt(4)
	s_sub_i32 s10, s36, 32
	v_cvt_pk_bf16_f32 v34, v34, v38
	s_cmp_lt_u32 s52, 61
	ds_write_b32 v169, v34 offset:57344
	v_cvt_pk_bf16_f32 v34, v35, v39
	s_cselect_b32 s10, s10, 0x7e0
	ds_write_b32 v169, v34 offset:57408
	v_cvt_pk_bf16_f32 v34, v36, v40
	s_lshl_b64 s[54:55], s[10:11], 11
	ds_write_b32 v169, v34 offset:57472
	v_cvt_pk_bf16_f32 v34, v37, v41
	ds_write_b32 v169, v34 offset:57536
	v_lshl_add_u64 v[38:39], v[156:157], 0, s[54:55]
	global_load_dwordx4 v[34:37], v[38:39], off sc1 nt
	v_lshl_add_u64 v[38:39], v[38:39], 0, s[22:23]
	global_load_dwordx4 v[38:41], v[38:39], off sc1 nt
	v_add_u32_e32 v52, v93, v165
	v_add_u32_e32 v94, v161, v164
	ds_read_b64 v[64:65], v52
	ds_read_b128 v[52:55], v94 offset:49152
	ds_read_b128 v[56:59], v94 offset:51200
	ds_read_b128 v[60:63], v94 offset:53248
	ds_read_b128 v[82:85], v94 offset:55296
	s_waitcnt lgkmcnt(0)
	v_cvt_pk_f32_fp8_e32 v[86:87], v64
	v_cvt_pk_f32_fp8_sdwa v[88:89], v64 src0_sel:WORD_1
	v_cvt_pk_f32_fp8_e32 v[90:91], v65
	v_cvt_pk_f32_fp8_sdwa v[64:65], v65 src0_sel:WORD_1
	v_cvt_pk_bf16_f32 v86, v86, v87
	v_cvt_pk_bf16_f32 v87, v88, v89
	v_cvt_pk_bf16_f32 v88, v90, v91
	v_cvt_pk_bf16_f32 v89, v64, v65
	s_nop 0
	v_mfma_f32_32x32x16_bf16 v[114:129], v[52:55], v[86:89], v[114:129]
	v_mfma_f32_32x32x16_bf16 v[18:33], v[56:59], v[86:89], v[18:33]
	v_mfma_f32_32x32x16_bf16 v[66:81], v[60:63], v[86:89], v[66:81]
	v_mfma_f32_32x32x16_bf16 v[2:17], v[82:85], v[86:89], v[2:17]
	s_waitcnt vmcnt(5)
	s_mov_b32 m0, s56
	s_waitcnt lgkmcnt(0)
	s_barrier
	v_lshl_add_u64 v[52:53], v[50:51], 0, s[10:11]
	global_load_lds_dwordx4 v[52:53], off
	s_addk_i32 s53, 0x402
	s_bfe_u32 s10, s53, 0x70009
	s_mul_i32 s10, s10, 3
	s_sub_i32 s10, s37, s10
	s_add_i32 s10, s10, 6
	s_and_b32 s10, s10, 0xff
	s_lshl_b32 s10, s10, 14
	s_add_i32 s37, s39, s10
	v_add_u32_e32 v93, s37, v160
	v_add_u32_e32 v52, v93, v163
	ds_read_b64 v[64:65], v52
	ds_read_b128 v[52:55], v92 offset:57344
	ds_read_b128 v[56:59], v92 offset:59392
	ds_read_b128 v[60:63], v92 offset:61440
	ds_read_b128 v[82:85], v92 offset:63488
	s_waitcnt lgkmcnt(0)
	v_cvt_pk_f32_fp8_e32 v[86:87], v64
	v_cvt_pk_f32_fp8_sdwa v[88:89], v64 src0_sel:WORD_1
	v_cvt_pk_f32_fp8_e32 v[90:91], v65
	v_cvt_pk_f32_fp8_sdwa v[64:65], v65 src0_sel:WORD_1
	v_cvt_pk_bf16_f32 v86, v86, v87
	v_cvt_pk_bf16_f32 v87, v88, v89
	v_cvt_pk_bf16_f32 v88, v90, v91
	v_cvt_pk_bf16_f32 v89, v64, v65
	s_nop 1
	v_mfma_f32_32x32x16_bf16 v[114:129], v[52:55], v[86:89], v[114:129]
	v_mfma_f32_32x32x16_bf16 v[18:33], v[56:59], v[86:89], v[18:33]
	v_mfma_f32_32x32x16_bf16 v[66:81], v[60:63], v[86:89], v[66:81]
	v_mfma_f32_32x32x16_bf16 v[2:17], v[82:85], v[86:89], v[2:17]
	s_waitcnt vmcnt(4)
	s_cmp_lt_u32 s52, 60
	v_cvt_pk_bf16_f32 v42, v42, v46
	ds_write_b32 v169, v42 offset:49152
	v_cvt_pk_bf16_f32 v42, v43, v47
	s_cselect_b32 s10, s36, 0x7e0
	ds_write_b32 v169, v42 offset:49216
	v_cvt_pk_bf16_f32 v42, v44, v48
	s_lshl_b64 s[54:55], s[10:11], 11
	ds_write_b32 v169, v42 offset:49280
	v_cvt_pk_bf16_f32 v42, v45, v49
	ds_write_b32 v169, v42 offset:49344
	v_lshl_add_u64 v[46:47], v[156:157], 0, s[54:55]
	global_load_dwordx4 v[42:45], v[46:47], off sc1 nt
	v_lshl_add_u64 v[46:47], v[46:47], 0, s[22:23]
	global_load_dwordx4 v[46:49], v[46:47], off sc1 nt
	v_add_u32_e32 v52, v93, v165
	ds_read_b64 v[64:65], v52
	ds_read_b128 v[52:55], v94 offset:57344
	ds_read_b128 v[56:59], v94 offset:59392
	ds_read_b128 v[60:63], v94 offset:61440
	ds_read_b128 v[82:85], v94 offset:63488
	s_waitcnt lgkmcnt(0)
	v_cvt_pk_f32_fp8_e32 v[86:87], v64
	v_cvt_pk_f32_fp8_sdwa v[88:89], v64 src0_sel:WORD_1
	v_cvt_pk_f32_fp8_e32 v[90:91], v65
	v_cvt_pk_f32_fp8_sdwa v[64:65], v65 src0_sel:WORD_1
	v_cvt_pk_bf16_f32 v86, v86, v87
	v_cvt_pk_bf16_f32 v87, v88, v89
	v_cvt_pk_bf16_f32 v88, v90, v91
	v_cvt_pk_bf16_f32 v89, v64, v65
	s_nop 0
	v_mfma_f32_32x32x16_bf16 v[114:129], v[52:55], v[86:89], v[114:129]
	v_mfma_f32_32x32x16_bf16 v[18:33], v[56:59], v[86:89], v[18:33]
	v_mfma_f32_32x32x16_bf16 v[66:81], v[60:63], v[86:89], v[66:81]
	v_mfma_f32_32x32x16_bf16 v[2:17], v[82:85], v[86:89], v[2:17]
	s_waitcnt vmcnt(5)
	s_mov_b32 m0, s37
	s_waitcnt lgkmcnt(0)
	s_barrier
	v_lshl_add_u64 v[52:53], v[50:51], 0, s[10:11]
	global_load_lds_dwordx4 v[52:53], off
	s_add_i32 s36, s36, 64
	s_cmp_gt_u32 s52, 61
	s_mov_b32 s37, s52
	s_cbranch_scc0 .Lmoe_G2_1015
	s_branch .Lmoe_X_1015
.Lmoe_G3_1015:
	s_mul_i32 s53, s37, 0xab
	s_add_i32 s10, s53, 0x357
	s_bfe_u32 s10, s10, 0x70009
	s_mul_i32 s10, s10, 3
	s_sub_i32 s10, s37, s10
	s_add_i32 s10, s10, 5
	s_and_b32 s10, s10, 0xff
	s_lshl_b32 s10, s10, 14
	s_add_i32 s56, s39, s10
	s_add_i32 s52, s37, 2
	v_add_u32_e32 v93, s56, v160
	v_add_u32_e32 v52, v93, v163
	v_add_u32_e32 v92, v161, v162
	ds_read_b64 v[64:65], v52
	ds_read_b128 v[52:55], v92 offset:49152
	ds_read_b128 v[56:59], v92 offset:51200
	ds_read_b128 v[60:63], v92 offset:53248
	ds_read_b128 v[82:85], v92 offset:55296
	s_waitcnt lgkmcnt(0)
	v_cvt_pk_f32_fp8_e32 v[86:87], v64
	v_cvt_pk_f32_fp8_sdwa v[88:89], v64 src0_sel:WORD_1
	v_cvt_pk_f32_fp8_e32 v[90:91], v65
	v_cvt_pk_f32_fp8_sdwa v[64:65], v65 src0_sel:WORD_1
	v_cvt_pk_bf16_f32 v86, v86, v87
	v_cvt_pk_bf16_f32 v87, v88, v89
	v_cvt_pk_bf16_f32 v88, v90, v91
	v_cvt_pk_bf16_f32 v89, v64, v65
	s_nop 1
	v_mfma_f32_32x32x16_bf16 v[114:129], v[52:55], v[86:89], v[114:129]
	v_mfma_f32_32x32x16_bf16 v[18:33], v[56:59], v[86:89], v[18:33]
	v_mfma_f32_32x32x16_bf16 v[66:81], v[60:63], v[86:89], v[66:81]
	v_mfma_f32_32x32x16_bf16 v[2:17], v[82:85], v[86:89], v[2:17]
	v_add_u32_e32 v52, v93, v165
	v_add_u32_e32 v94, v161, v164
	ds_read_b64 v[64:65], v52
	ds_read_b128 v[52:55], v94 offset:49152
	ds_read_b128 v[56:59], v94 offset:51200
	ds_read_b128 v[60:63], v94 offset:53248
	ds_read_b128 v[82:85], v94 offset:55296
	s_waitcnt lgkmcnt(0)
	v_cvt_pk_f32_fp8_e32 v[86:87], v64
	v_cvt_pk_f32_fp8_sdwa v[88:89], v64 src0_sel:WORD_1
	v_cvt_pk_f32_fp8_e32 v[90:91], v65
	v_cvt_pk_f32_fp8_sdwa v[64:65], v65 src0_sel:WORD_1
	v_cvt_pk_bf16_f32 v86, v86, v87
	v_cvt_pk_bf16_f32 v87, v88, v89
	v_cvt_pk_bf16_f32 v88, v90, v91
	v_cvt_pk_bf16_f32 v89, v64, v65
	s_nop 0
	v_mfma_f32_32x32x16_bf16 v[114:129], v[52:55], v[86:89], v[114:129]
	v_mfma_f32_32x32x16_bf16 v[18:33], v[56:59], v[86:89], v[18:33]
	v_mfma_f32_32x32x16_bf16 v[66:81], v[60:63], v[86:89], v[66:81]
	v_mfma_f32_32x32x16_bf16 v[2:17], v[82:85], v[86:89], v[2:17]
	s_waitcnt vmcnt(4)
	s_sub_i32 s10, s36, 32
	v_cvt_pk_bf16_f32 v34, v34, v38
	s_cmp_lt_u32 s52, 61
	ds_write_b32 v169, v34 offset:57344
	v_cvt_pk_bf16_f32 v34, v35, v39
	s_cselect_b32 s10, s10, 0x7e0
	ds_write_b32 v169, v34 offset:57408
	v_cvt_pk_bf16_f32 v34, v36, v40
	s_lshl_b64 s[54:55], s[10:11], 11
	ds_write_b32 v169, v34 offset:57472
	v_cvt_pk_bf16_f32 v34, v37, v41
	ds_write_b32 v169, v34 offset:57536
	v_lshl_add_u64 v[38:39], v[156:157], 0, s[54:55]
	global_load_dwordx4 v[34:37], v[38:39], off sc1 nt
	v_lshl_add_u64 v[38:39], v[38:39], 0, s[22:23]
	global_load_dwordx4 v[38:41], v[38:39], off sc1 nt
	s_waitcnt vmcnt(5)
	s_mov_b32 m0, s56
	s_waitcnt lgkmcnt(0)
	s_barrier
	v_lshl_add_u64 v[52:53], v[50:51], 0, s[10:11]
	global_load_lds_dwordx4 v[52:53], off
	s_addk_i32 s53, 0x402
	s_bfe_u32 s10, s53, 0x70009
	s_mul_i32 s10, s10, 3
	s_sub_i32 s10, s37, s10
	s_add_i32 s10, s10, 6
	s_and_b32 s10, s10, 0xff
	s_lshl_b32 s10, s10, 14
	s_add_i32 s37, s39, s10
	v_add_u32_e32 v93, s37, v160
	v_add_u32_e32 v52, v93, v163
	ds_read_b64 v[64:65], v52
	ds_read_b128 v[52:55], v92 offset:57344
	ds_read_b128 v[56:59], v92 offset:59392
	ds_read_b128 v[60:63], v92 offset:61440
	ds_read_b128 v[82:85], v92 offset:63488
	s_waitcnt lgkmcnt(0)
	v_cvt_pk_f32_fp8_e32 v[86:87], v64
	v_cvt_pk_f32_fp8_sdwa v[88:89], v64 src0_sel:WORD_1
	v_cvt_pk_f32_fp8_e32 v[90:91], v65
	v_cvt_pk_f32_fp8_sdwa v[64:65], v65 src0_sel:WORD_1
	v_cvt_pk_bf16_f32 v86, v86, v87
	v_cvt_pk_bf16_f32 v87, v88, v89
	v_cvt_pk_bf16_f32 v88, v90, v91
	v_cvt_pk_bf16_f32 v89, v64, v65
	s_nop 1
	v_mfma_f32_32x32x16_bf16 v[114:129], v[52:55], v[86:89], v[114:129]
	v_mfma_f32_32x32x16_bf16 v[18:33], v[56:59], v[86:89], v[18:33]
	v_mfma_f32_32x32x16_bf16 v[66:81], v[60:63], v[86:89], v[66:81]
	v_mfma_f32_32x32x16_bf16 v[2:17], v[82:85], v[86:89], v[2:17]
	v_add_u32_e32 v52, v93, v165
	ds_read_b64 v[64:65], v52
	ds_read_b128 v[52:55], v94 offset:57344
	ds_read_b128 v[56:59], v94 offset:59392
	ds_read_b128 v[60:63], v94 offset:61440
	ds_read_b128 v[82:85], v94 offset:63488
	s_waitcnt lgkmcnt(0)
	v_cvt_pk_f32_fp8_e32 v[86:87], v64
	v_cvt_pk_f32_fp8_sdwa v[88:89], v64 src0_sel:WORD_1
	v_cvt_pk_f32_fp8_e32 v[90:91], v65
	v_cvt_pk_f32_fp8_sdwa v[64:65], v65 src0_sel:WORD_1
	v_cvt_pk_bf16_f32 v86, v86, v87
	v_cvt_pk_bf16_f32 v87, v88, v89
	v_cvt_pk_bf16_f32 v88, v90, v91
	v_cvt_pk_bf16_f32 v89, v64, v65
	s_nop 0
	v_mfma_f32_32x32x16_bf16 v[114:129], v[52:55], v[86:89], v[114:129]
	v_mfma_f32_32x32x16_bf16 v[18:33], v[56:59], v[86:89], v[18:33]
	v_mfma_f32_32x32x16_bf16 v[66:81], v[60:63], v[86:89], v[66:81]
	v_mfma_f32_32x32x16_bf16 v[2:17], v[82:85], v[86:89], v[2:17]
	s_waitcnt vmcnt(4)
	s_cmp_lt_u32 s52, 60
	v_cvt_pk_bf16_f32 v42, v42, v46
	ds_write_b32 v169, v42 offset:49152
	v_cvt_pk_bf16_f32 v42, v43, v47
	s_cselect_b32 s10, s36, 0x7e0
	ds_write_b32 v169, v42 offset:49216
	v_cvt_pk_bf16_f32 v42, v44, v48
	s_lshl_b64 s[54:55], s[10:11], 11
	ds_write_b32 v169, v42 offset:49280
	v_cvt_pk_bf16_f32 v42, v45, v49
	ds_write_b32 v169, v42 offset:49344
	v_lshl_add_u64 v[46:47], v[156:157], 0, s[54:55]
	global_load_dwordx4 v[42:45], v[46:47], off sc1 nt
	v_lshl_add_u64 v[46:47], v[46:47], 0, s[22:23]
	global_load_dwordx4 v[46:49], v[46:47], off sc1 nt
	s_waitcnt vmcnt(5)
	s_mov_b32 m0, s37
	s_waitcnt lgkmcnt(0)
	s_barrier
	v_lshl_add_u64 v[52:53], v[50:51], 0, s[10:11]
	global_load_lds_dwordx4 v[52:53], off
	s_add_i32 s36, s36, 64
	s_cmp_gt_u32 s52, 61
	s_mov_b32 s37, s52
	s_cbranch_scc0 .Lmoe_G3_1015

.LBB0_1017:
	v_mov_b32_e32 v97, 0
	s_and_b64 vcc, exec, s[36:37]
	v_mov_b32_e32 v96, v97
	v_mov_b32_e32 v95, v97
	v_mov_b32_e32 v94, v97
	v_mov_b32_e32 v93, v97
	v_mov_b32_e32 v92, v97
	v_mov_b32_e32 v91, v97
	v_mov_b32_e32 v90, v97
	v_mov_b32_e32 v89, v97
	v_mov_b32_e32 v88, v97
	v_mov_b32_e32 v87, v97
	v_mov_b32_e32 v86, v97
	v_mov_b32_e32 v85, v97
	v_mov_b32_e32 v84, v97
	v_mov_b32_e32 v83, v97
	v_mov_b32_e32 v82, v97
	v_mov_b32_e32 v65, v97
	v_mov_b32_e32 v64, v97
	v_mov_b32_e32 v63, v97
	v_mov_b32_e32 v62, v97
	v_mov_b32_e32 v61, v97
	v_mov_b32_e32 v60, v97
	v_mov_b32_e32 v59, v97
	v_mov_b32_e32 v58, v97
	v_mov_b32_e32 v57, v97
	v_mov_b32_e32 v56, v97
	v_mov_b32_e32 v55, v97
	v_mov_b32_e32 v54, v97
	v_mov_b32_e32 v53, v97
	v_mov_b32_e32 v52, v97
	v_mov_b32_e32 v51, v97
	v_mov_b32_e32 v50, v97
	v_mov_b32_e32 v113, v97
	v_mov_b32_e32 v112, v97
	v_mov_b32_e32 v111, v97
	v_mov_b32_e32 v110, v97
	v_mov_b32_e32 v109, v97
	v_mov_b32_e32 v108, v97
	v_mov_b32_e32 v107, v97
	v_mov_b32_e32 v106, v97
	v_mov_b32_e32 v105, v97
	v_mov_b32_e32 v104, v97
	v_mov_b32_e32 v103, v97
	v_mov_b32_e32 v102, v97
	v_mov_b32_e32 v101, v97
	v_mov_b32_e32 v100, v97
	v_mov_b32_e32 v99, v97
	v_mov_b32_e32 v98, v97
	v_mov_b32_e32 v49, v97
	v_mov_b32_e32 v48, v97
	v_mov_b32_e32 v47, v97
	v_mov_b32_e32 v46, v97
	v_mov_b32_e32 v45, v97
	v_mov_b32_e32 v44, v97
	v_mov_b32_e32 v43, v97
	v_mov_b32_e32 v42, v97
	v_mov_b32_e32 v41, v97
	v_mov_b32_e32 v40, v97
	v_mov_b32_e32 v39, v97
	v_mov_b32_e32 v38, v97
	v_mov_b32_e32 v37, v97
	v_mov_b32_e32 v36, v97
	v_mov_b32_e32 v35, v97
	v_mov_b32_e32 v34, v97
	s_cbranch_vccz .LBB0_1021
	global_load_dwordx4 v[2:5], v[156:157], off sc1 nt
	s_mov_b32 m0, s39
	global_load_dwordx4 v[6:9], v[132:133], off sc1 nt
	v_or_b32_e32 v158, v136, v1
	global_load_lds_dwordx4 v146, s[14:15]
	s_mov_b32 m0, s42
	v_mov_b32_e32 v159, v147
	global_load_lds_dwordx4 v158, s[14:15]
	global_load_dwordx4 v[130:133], v[130:131], off sc1 nt
	global_load_dwordx4 v[134:137], v[134:135], off sc1 nt
	s_mov_b32 m0, s40
	s_nop 0
	global_load_lds_dwordx4 v146, s[16:17]
	s_mov_b32 m0, s43
	s_nop 0
	global_load_lds_dwordx4 v158, s[16:17]
	s_waitcnt vmcnt(6)
	s_nop 0
	v_cvt_pk_bf16_f32 v2, v2, v6
	ds_write_b32 v169, v2 offset:49152
	v_cvt_pk_bf16_f32 v2, v3, v7
	ds_write_b32 v169, v2 offset:49216
	v_cvt_pk_bf16_f32 v2, v4, v8
	ds_write_b32 v169, v2 offset:49280
	v_cvt_pk_bf16_f32 v2, v5, v9
	ds_write_b32 v169, v2 offset:49344
	global_load_dwordx4 v[138:141], v[138:139], off sc1 nt
	global_load_dwordx4 v[142:145], v[142:143], off sc1 nt
	s_waitcnt vmcnt(6)
	s_mov_b32 m0, s41
	s_waitcnt lgkmcnt(0)
	s_barrier
	global_load_lds_dwordx4 v146, s[18:19]
	s_mov_b32 m0, s44
	v_mov_b32_e32 v34, 0
	global_load_lds_dwordx4 v158, s[18:19]
	s_mov_b32 s37, -2
	s_movk_i32 s36, 0x80
	v_mov_b32_e32 v35, v34
	v_mov_b32_e32 v36, v34
	v_mov_b32_e32 v37, v34
	v_mov_b32_e32 v38, v34
	v_mov_b32_e32 v39, v34
	v_mov_b32_e32 v40, v34
	v_mov_b32_e32 v41, v34
	v_mov_b32_e32 v42, v34
	v_mov_b32_e32 v43, v34
	v_mov_b32_e32 v44, v34
	v_mov_b32_e32 v45, v34
	v_mov_b32_e32 v46, v34
	v_mov_b32_e32 v47, v34
	v_mov_b32_e32 v48, v34
	v_mov_b32_e32 v49, v34
	v_mov_b32_e32 v98, v34
	v_mov_b32_e32 v99, v34
	v_mov_b32_e32 v100, v34
	v_mov_b32_e32 v101, v34
	v_mov_b32_e32 v102, v34
	v_mov_b32_e32 v103, v34
	v_mov_b32_e32 v104, v34
	v_mov_b32_e32 v105, v34
	v_mov_b32_e32 v106, v34
	v_mov_b32_e32 v107, v34
	v_mov_b32_e32 v108, v34
	v_mov_b32_e32 v109, v34
	v_mov_b32_e32 v110, v34
	v_mov_b32_e32 v111, v34
	v_mov_b32_e32 v112, v34
	v_mov_b32_e32 v113, v34
	v_mov_b32_e32 v50, v34
	v_mov_b32_e32 v51, v34
	v_mov_b32_e32 v52, v34
	v_mov_b32_e32 v53, v34
	v_mov_b32_e32 v54, v34
	v_mov_b32_e32 v55, v34
	v_mov_b32_e32 v56, v34
	v_mov_b32_e32 v57, v34
	v_mov_b32_e32 v58, v34
	v_mov_b32_e32 v59, v34
	v_mov_b32_e32 v60, v34
	v_mov_b32_e32 v61, v34
	v_mov_b32_e32 v62, v34
	v_mov_b32_e32 v63, v34
	v_mov_b32_e32 v64, v34
	v_mov_b32_e32 v65, v34
	v_mov_b32_e32 v82, v34
	v_mov_b32_e32 v83, v34
	v_mov_b32_e32 v84, v34
	v_mov_b32_e32 v85, v34
	v_mov_b32_e32 v86, v34
	v_mov_b32_e32 v87, v34
	v_mov_b32_e32 v88, v34
	v_mov_b32_e32 v89, v34
	v_mov_b32_e32 v90, v34
	v_mov_b32_e32 v91, v34
	v_mov_b32_e32 v92, v34
	v_mov_b32_e32 v93, v34
	v_mov_b32_e32 v94, v34
	v_mov_b32_e32 v95, v34
	v_mov_b32_e32 v96, v34
	v_mov_b32_e32 v97, v34
	v_mov_b32_e32 v2, v34
	v_mov_b32_e32 v3, v34
	v_mov_b32_e32 v4, v34
	v_mov_b32_e32 v5, v34
	v_mov_b32_e32 v6, v34
	v_mov_b32_e32 v7, v34
	v_mov_b32_e32 v8, v34
	v_mov_b32_e32 v9, v34
	v_mov_b32_e32 v10, v34
	v_mov_b32_e32 v11, v34
	v_mov_b32_e32 v12, v34
	v_mov_b32_e32 v13, v34
	v_mov_b32_e32 v14, v34
	v_mov_b32_e32 v15, v34
	v_mov_b32_e32 v16, v34
	v_mov_b32_e32 v17, v34
	v_mov_b32_e32 v66, v34
	v_mov_b32_e32 v67, v34
	v_mov_b32_e32 v68, v34
	v_mov_b32_e32 v69, v34
	v_mov_b32_e32 v70, v34
	v_mov_b32_e32 v71, v34
	v_mov_b32_e32 v72, v34
	v_mov_b32_e32 v73, v34
	v_mov_b32_e32 v74, v34
	v_mov_b32_e32 v75, v34
	v_mov_b32_e32 v76, v34
	v_mov_b32_e32 v77, v34
	v_mov_b32_e32 v78, v34
	v_mov_b32_e32 v79, v34
	v_mov_b32_e32 v80, v34
	v_mov_b32_e32 v81, v34
	v_mov_b32_e32 v18, v34
	v_mov_b32_e32 v19, v34
	v_mov_b32_e32 v20, v34
	v_mov_b32_e32 v21, v34
	v_mov_b32_e32 v22, v34
	v_mov_b32_e32 v23, v34
	v_mov_b32_e32 v24, v34
	v_mov_b32_e32 v25, v34
	v_mov_b32_e32 v26, v34
	v_mov_b32_e32 v27, v34
	v_mov_b32_e32 v28, v34
	v_mov_b32_e32 v29, v34
	v_mov_b32_e32 v30, v34
	v_mov_b32_e32 v31, v34
	v_mov_b32_e32 v32, v34
	v_mov_b32_e32 v33, v34
	v_mov_b32_e32 v114, v34
	v_mov_b32_e32 v115, v34
	v_mov_b32_e32 v116, v34
	v_mov_b32_e32 v117, v34
	v_mov_b32_e32 v118, v34
	v_mov_b32_e32 v119, v34
	v_mov_b32_e32 v120, v34
	v_mov_b32_e32 v121, v34
	v_mov_b32_e32 v122, v34
	v_mov_b32_e32 v123, v34
	v_mov_b32_e32 v124, v34
	v_mov_b32_e32 v125, v34
	v_mov_b32_e32 v126, v34
	v_mov_b32_e32 v127, v34
	v_mov_b32_e32 v128, v34
	v_mov_b32_e32 v129, v34
	v_readfirstlane_b32 s98, v250
	s_bfe_u32 s98, s98, 0x20006
	s_cmp_eq_u32 s98, 1
	s_cbranch_scc1 .Lmoe_G1_1019
	s_cmp_eq_u32 s98, 2
	s_cbranch_scc1 .Lmoe_G2_1019
	s_cmp_eq_u32 s98, 3
	s_cbranch_scc1 .Lmoe_G3_1019
.LBB0_1019:
	s_mul_i32 s53, s37, 0xab
	s_add_i32 s10, s53, 0x357
	s_bfe_u32 s10, s10, 0x70009
	s_mul_i32 s10, s10, 3
	s_sub_i32 s10, s37, s10
	s_add_i32 s10, s10, 5
	s_and_b32 s10, s10, 0xff
	s_lshl_b32 s10, s10, 14
	s_add_i32 s54, s39, s10
	s_add_i32 s52, s37, 2
	s_waitcnt vmcnt(6)
	s_sub_i32 s10, s36, 32
	v_cvt_pk_bf16_f32 v130, v130, v134
	s_cmp_lt_u32 s52, 61
	ds_write_b32 v169, v130 offset:57344
	v_cvt_pk_bf16_f32 v130, v131, v135
	s_cselect_b32 s10, s10, 0x7e0
	ds_write_b32 v169, v130 offset:57408
	v_cvt_pk_bf16_f32 v130, v132, v136
	s_lshl_b64 s[56:57], s[10:11], 11
	ds_write_b32 v169, v130 offset:57472
	v_cvt_pk_bf16_f32 v130, v133, v137
	ds_write_b32 v169, v130 offset:57536
	v_lshl_add_u64 v[134:135], v[156:157], 0, s[56:57]
	global_load_dwordx4 v[130:133], v[134:135], off sc1 nt
	v_lshl_add_u64 v[134:135], v[134:135], 0, s[22:23]
	global_load_dwordx4 v[134:137], v[134:135], off sc1 nt
	v_add_u32_e32 v171, s54, v160
	v_add_u32_e32 v198, v171, v163
	v_add_u32_e32 v154, v161, v162
	ds_read_b64 v[188:189], v198
	ds_read_b128 v[172:175], v154 offset:49152
	ds_read_b128 v[176:179], v154 offset:51200
	ds_read_b128 v[180:183], v154 offset:53248
	ds_read_b128 v[184:187], v154 offset:55296
	s_waitcnt lgkmcnt(0)
	v_cvt_pk_f32_fp8_e32 v[190:191], v188
	v_cvt_pk_f32_fp8_sdwa v[192:193], v188 src0_sel:WORD_1
	v_cvt_pk_f32_fp8_e32 v[194:195], v189
	v_cvt_pk_f32_fp8_sdwa v[196:197], v189 src0_sel:WORD_1
	v_cvt_pk_bf16_f32 v188, v190, v191
	v_cvt_pk_bf16_f32 v189, v192, v193
	v_cvt_pk_bf16_f32 v190, v194, v195
	v_cvt_pk_bf16_f32 v191, v196, v197
	ds_read_b64 v[192:193], v198 offset:8192
	s_waitcnt lgkmcnt(0)
	v_cvt_pk_f32_fp8_e32 v[194:195], v192
	v_cvt_pk_f32_fp8_sdwa v[196:197], v192 src0_sel:WORD_1
	v_cvt_pk_f32_fp8_e32 v[198:199], v193
	v_cvt_pk_f32_fp8_sdwa v[200:201], v193 src0_sel:WORD_1
	v_cvt_pk_bf16_f32 v192, v194, v195
	v_cvt_pk_bf16_f32 v193, v196, v197
	v_cvt_pk_bf16_f32 v194, v198, v199
	v_cvt_pk_bf16_f32 v195, v200, v201
	s_nop 1
	v_mfma_f32_32x32x16_bf16 v[114:129], v[172:175], v[188:191], v[114:129]
	v_mfma_f32_32x32x16_bf16 v[18:33], v[176:179], v[188:191], v[18:33]
	v_mfma_f32_32x32x16_bf16 v[66:81], v[180:183], v[188:191], v[66:81]
	v_mfma_f32_32x32x16_bf16 v[2:17], v[184:187], v[188:191], v[2:17]
	v_mfma_f32_32x32x16_bf16 v[82:97], v[172:175], v[192:195], v[82:97]
	v_mfma_f32_32x32x16_bf16 v[50:65], v[176:179], v[192:195], v[50:65]
	v_mfma_f32_32x32x16_bf16 v[98:113], v[180:183], v[192:195], v[98:113]
	v_mfma_f32_32x32x16_bf16 v[34:49], v[184:187], v[192:195], v[34:49]
	v_add_u32_e32 v171, v171, v165
	v_add_u32_e32 v202, v161, v164
	ds_read_b64 v[188:189], v171
	ds_read_b128 v[172:175], v202 offset:49152
	ds_read_b128 v[176:179], v202 offset:51200
	ds_read_b128 v[180:183], v202 offset:53248
	ds_read_b128 v[184:187], v202 offset:55296
	s_waitcnt lgkmcnt(0)
	v_cvt_pk_f32_fp8_e32 v[190:191], v188
	v_cvt_pk_f32_fp8_sdwa v[192:193], v188 src0_sel:WORD_1
	v_cvt_pk_f32_fp8_e32 v[194:195], v189
	v_cvt_pk_f32_fp8_sdwa v[196:197], v189 src0_sel:WORD_1
	v_cvt_pk_bf16_f32 v188, v190, v191
	v_cvt_pk_bf16_f32 v189, v192, v193
	v_cvt_pk_bf16_f32 v190, v194, v195
	v_cvt_pk_bf16_f32 v191, v196, v197
	ds_read_b64 v[192:193], v171 offset:8192
	v_mfma_f32_32x32x16_bf16 v[114:129], v[172:175], v[188:191], v[114:129]
	s_waitcnt lgkmcnt(0)
	v_cvt_pk_f32_fp8_e32 v[194:195], v192
	v_cvt_pk_f32_fp8_e32 v[196:197], v193
	v_mfma_f32_32x32x16_bf16 v[18:33], v[176:179], v[188:191], v[18:33]
	v_mfma_f32_32x32x16_bf16 v[66:81], v[180:183], v[188:191], v[66:81]
	v_mfma_f32_32x32x16_bf16 v[2:17], v[184:187], v[188:191], v[2:17]
	v_cvt_pk_f32_fp8_sdwa v[190:191], v192 src0_sel:WORD_1
	v_cvt_pk_f32_fp8_sdwa v[192:193], v193 src0_sel:WORD_1
	v_cvt_pk_bf16_f32 v188, v194, v195
	v_cvt_pk_bf16_f32 v189, v190, v191
	v_cvt_pk_bf16_f32 v190, v196, v197
	v_cvt_pk_bf16_f32 v191, v192, v193
	s_nop 0
	v_mfma_f32_32x32x16_bf16 v[82:97], v[172:175], v[188:191], v[82:97]
	v_mfma_f32_32x32x16_bf16 v[50:65], v[176:179], v[188:191], v[50:65]
	v_mfma_f32_32x32x16_bf16 v[98:113], v[180:183], v[188:191], v[98:113]
	v_mfma_f32_32x32x16_bf16 v[34:49], v[184:187], v[188:191], v[34:49]
	s_add_u32 s56, s14, s10
	s_waitcnt vmcnt(6)
	s_addc_u32 s57, s15, 0
	s_mov_b32 m0, s54
	s_waitcnt lgkmcnt(0)
	s_barrier
	v_lshl_add_u64 v[172:173], s[56:57], 0, v[146:147]
	global_load_lds_dwordx4 v[172:173], off
	v_lshl_add_u64 v[172:173], s[56:57], 0, v[158:159]
	s_add_i32 m0, s54, 0x2000
	s_addk_i32 s53, 0x402
	global_load_lds_dwordx4 v[172:173], off
	s_bfe_u32 s10, s53, 0x70009
	s_mul_i32 s10, s10, 3
	s_sub_i32 s10, s37, s10
	s_add_i32 s10, s10, 6
	s_and_b32 s10, s10, 0xff
	s_lshl_b32 s10, s10, 14
	s_add_i32 s37, s39, s10
	s_waitcnt vmcnt(6)
	s_cmp_lt_u32 s52, 60
	v_cvt_pk_bf16_f32 v138, v138, v142
	ds_write_b32 v169, v138 offset:49152
	v_cvt_pk_bf16_f32 v138, v139, v143
	s_cselect_b32 s10, s36, 0x7e0
	ds_write_b32 v169, v138 offset:49216
	v_cvt_pk_bf16_f32 v138, v140, v144
	s_lshl_b64 s[54:55], s[10:11], 11
	ds_write_b32 v169, v138 offset:49280
	v_cvt_pk_bf16_f32 v138, v141, v145
	ds_write_b32 v169, v138 offset:49344
	v_lshl_add_u64 v[142:143], v[156:157], 0, s[54:55]
	global_load_dwordx4 v[138:141], v[142:143], off sc1 nt
	v_lshl_add_u64 v[142:143], v[142:143], 0, s[22:23]
	global_load_dwordx4 v[142:145], v[142:143], off sc1 nt
	v_add_u32_e32 v171, s37, v160
	v_add_u32_e32 v198, v171, v163
	ds_read_b64 v[188:189], v198
	ds_read_b128 v[172:175], v154 offset:57344
	ds_read_b128 v[176:179], v154 offset:59392
	ds_read_b128 v[180:183], v154 offset:61440
	ds_read_b128 v[184:187], v154 offset:63488
	s_waitcnt lgkmcnt(0)
	v_cvt_pk_f32_fp8_e32 v[190:191], v188
	v_cvt_pk_f32_fp8_sdwa v[192:193], v188 src0_sel:WORD_1
	v_cvt_pk_f32_fp8_e32 v[194:195], v189
	v_cvt_pk_f32_fp8_sdwa v[196:197], v189 src0_sel:WORD_1
	v_cvt_pk_bf16_f32 v188, v190, v191
	v_cvt_pk_bf16_f32 v189, v192, v193
	v_cvt_pk_bf16_f32 v190, v194, v195
	v_cvt_pk_bf16_f32 v191, v196, v197
	ds_read_b64 v[192:193], v198 offset:8192
	s_waitcnt lgkmcnt(0)
	v_cvt_pk_f32_fp8_e32 v[194:195], v192
	v_cvt_pk_f32_fp8_sdwa v[196:197], v192 src0_sel:WORD_1
	v_cvt_pk_f32_fp8_e32 v[198:199], v193
	v_cvt_pk_f32_fp8_sdwa v[200:201], v193 src0_sel:WORD_1
	v_cvt_pk_bf16_f32 v192, v194, v195
	v_cvt_pk_bf16_f32 v193, v196, v197
	v_cvt_pk_bf16_f32 v194, v198, v199
	v_cvt_pk_bf16_f32 v195, v200, v201
	s_nop 1
	v_mfma_f32_32x32x16_bf16 v[114:129], v[172:175], v[188:191], v[114:129]
	v_mfma_f32_32x32x16_bf16 v[18:33], v[176:179], v[188:191], v[18:33]
	v_mfma_f32_32x32x16_bf16 v[66:81], v[180:183], v[188:191], v[66:81]
	v_mfma_f32_32x32x16_bf16 v[2:17], v[184:187], v[188:191], v[2:17]
	v_mfma_f32_32x32x16_bf16 v[82:97], v[172:175], v[192:195], v[82:97]
	v_mfma_f32_32x32x16_bf16 v[50:65], v[176:179], v[192:195], v[50:65]
	v_mfma_f32_32x32x16_bf16 v[98:113], v[180:183], v[192:195], v[98:113]
	v_mfma_f32_32x32x16_bf16 v[34:49], v[184:187], v[192:195], v[34:49]
	v_add_u32_e32 v154, v171, v165
	ds_read_b64 v[188:189], v154
	ds_read_b128 v[172:175], v202 offset:57344
	ds_read_b128 v[176:179], v202 offset:59392
	ds_read_b128 v[180:183], v202 offset:61440
	ds_read_b128 v[184:187], v202 offset:63488
	s_waitcnt lgkmcnt(0)
	v_cvt_pk_f32_fp8_e32 v[190:191], v188
	v_cvt_pk_f32_fp8_sdwa v[192:193], v188 src0_sel:WORD_1
	v_cvt_pk_f32_fp8_e32 v[194:195], v189
	v_cvt_pk_f32_fp8_sdwa v[196:197], v189 src0_sel:WORD_1
	v_cvt_pk_bf16_f32 v188, v190, v191
	v_cvt_pk_bf16_f32 v189, v192, v193
	v_cvt_pk_bf16_f32 v190, v194, v195
	v_cvt_pk_bf16_f32 v191, v196, v197
	ds_read_b64 v[192:193], v154 offset:8192
	v_mfma_f32_32x32x16_bf16 v[114:129], v[172:175], v[188:191], v[114:129]
	s_waitcnt lgkmcnt(0)
	v_cvt_pk_f32_fp8_e32 v[194:195], v192
	v_cvt_pk_f32_fp8_e32 v[196:197], v193
	v_mfma_f32_32x32x16_bf16 v[18:33], v[176:179], v[188:191], v[18:33]
	v_mfma_f32_32x32x16_bf16 v[66:81], v[180:183], v[188:191], v[66:81]
	v_mfma_f32_32x32x16_bf16 v[2:17], v[184:187], v[188:191], v[2:17]
	v_cvt_pk_f32_fp8_sdwa v[190:191], v192 src0_sel:WORD_1
	v_cvt_pk_f32_fp8_sdwa v[192:193], v193 src0_sel:WORD_1
	v_cvt_pk_bf16_f32 v188, v194, v195
	v_cvt_pk_bf16_f32 v189, v190, v191
	v_cvt_pk_bf16_f32 v190, v196, v197
	v_cvt_pk_bf16_f32 v191, v192, v193
	s_nop 0
	v_mfma_f32_32x32x16_bf16 v[82:97], v[172:175], v[188:191], v[82:97]
	v_mfma_f32_32x32x16_bf16 v[50:65], v[176:179], v[188:191], v[50:65]
	v_mfma_f32_32x32x16_bf16 v[98:113], v[180:183], v[188:191], v[98:113]
	v_mfma_f32_32x32x16_bf16 v[34:49], v[184:187], v[188:191], v[34:49]
	s_add_u32 s54, s14, s10
	s_waitcnt vmcnt(6)
	s_addc_u32 s55, s15, 0
	s_mov_b32 m0, s37
	s_waitcnt lgkmcnt(0)
	s_barrier
	v_lshl_add_u64 v[172:173], s[54:55], 0, v[146:147]
	global_load_lds_dwordx4 v[172:173], off
	v_lshl_add_u64 v[172:173], s[54:55], 0, v[158:159]
	s_add_i32 m0, s37, 0x2000
	s_add_i32 s36, s36, 64
	global_load_lds_dwordx4 v[172:173], off
	s_cmp_gt_u32 s52, 61
	s_mov_b32 s37, s52
	s_cbranch_scc0 .LBB0_1019
	s_branch .Lmoe_X_1019

.Lmoe_G2_1019:
	s_mul_i32 s53, s37, 0xab
	s_add_i32 s10, s53, 0x357
	s_bfe_u32 s10, s10, 0x70009
	s_mul_i32 s10, s10, 3
	s_sub_i32 s10, s37, s10
	s_add_i32 s10, s10, 5
	s_and_b32 s10, s10, 0xff
	s_lshl_b32 s10, s10, 14
	s_add_i32 s54, s39, s10
	s_add_i32 s52, s37, 2
	v_add_u32_e32 v171, s54, v160
	v_add_u32_e32 v198, v171, v163
	v_add_u32_e32 v154, v161, v162
	ds_read_b64 v[188:189], v198
	ds_read_b128 v[172:175], v154 offset:49152
	ds_read_b128 v[176:179], v154 offset:51200
	ds_read_b128 v[180:183], v154 offset:53248
	ds_read_b128 v[184:187], v154 offset:55296
	s_waitcnt lgkmcnt(0)
	v_cvt_pk_f32_fp8_e32 v[190:191], v188
	v_cvt_pk_f32_fp8_sdwa v[192:193], v188 src0_sel:WORD_1
	v_cvt_pk_f32_fp8_e32 v[194:195], v189
	v_cvt_pk_f32_fp8_sdwa v[196:197], v189 src0_sel:WORD_1
	v_cvt_pk_bf16_f32 v188, v190, v191
	v_cvt_pk_bf16_f32 v189, v192, v193
	v_cvt_pk_bf16_f32 v190, v194, v195
	v_cvt_pk_bf16_f32 v191, v196, v197
	ds_read_b64 v[192:193], v198 offset:8192
	s_waitcnt lgkmcnt(0)
	v_cvt_pk_f32_fp8_e32 v[194:195], v192
	v_cvt_pk_f32_fp8_sdwa v[196:197], v192 src0_sel:WORD_1
	v_cvt_pk_f32_fp8_e32 v[198:199], v193
	v_cvt_pk_f32_fp8_sdwa v[200:201], v193 src0_sel:WORD_1
	v_cvt_pk_bf16_f32 v192, v194, v195
	v_cvt_pk_bf16_f32 v193, v196, v197
	v_cvt_pk_bf16_f32 v194, v198, v199
	v_cvt_pk_bf16_f32 v195, v200, v201
	s_nop 1
	v_mfma_f32_32x32x16_bf16 v[114:129], v[172:175], v[188:191], v[114:129]
	v_mfma_f32_32x32x16_bf16 v[18:33], v[176:179], v[188:191], v[18:33]
	v_mfma_f32_32x32x16_bf16 v[66:81], v[180:183], v[188:191], v[66:81]
	v_mfma_f32_32x32x16_bf16 v[2:17], v[184:187], v[188:191], v[2:17]
	v_mfma_f32_32x32x16_bf16 v[82:97], v[172:175], v[192:195], v[82:97]
	v_mfma_f32_32x32x16_bf16 v[50:65], v[176:179], v[192:195], v[50:65]
	v_mfma_f32_32x32x16_bf16 v[98:113], v[180:183], v[192:195], v[98:113]
	v_mfma_f32_32x32x16_bf16 v[34:49], v[184:187], v[192:195], v[34:49]
	s_waitcnt vmcnt(6)
	s_sub_i32 s10, s36, 32
	v_cvt_pk_bf16_f32 v130, v130, v134
	s_cmp_lt_u32 s52, 61
	ds_write_b32 v169, v130 offset:57344
	v_cvt_pk_bf16_f32 v130, v131, v135
	s_cselect_b32 s10, s10, 0x7e0
	ds_write_b32 v169, v130 offset:57408
	v_cvt_pk_bf16_f32 v130, v132, v136
	s_lshl_b64 s[56:57], s[10:11], 11
	ds_write_b32 v169, v130 offset:57472
	v_cvt_pk_bf16_f32 v130, v133, v137
	ds_write_b32 v169, v130 offset:57536
	v_lshl_add_u64 v[134:135], v[156:157], 0, s[56:57]
	global_load_dwordx4 v[130:133], v[134:135], off sc1 nt
	v_lshl_add_u64 v[134:135], v[134:135], 0, s[22:23]
	global_load_dwordx4 v[134:137], v[134:135], off sc1 nt
	v_add_u32_e32 v171, v171, v165
	v_add_u32_e32 v202, v161, v164
	ds_read_b64 v[188:189], v171
	ds_read_b128 v[172:175], v202 offset:49152
	ds_read_b128 v[176:179], v202 offset:51200
	ds_read_b128 v[180:183], v202 offset:53248
	ds_read_b128 v[184:187], v202 offset:55296
	s_waitcnt lgkmcnt(0)
	v_cvt_pk_f32_fp8_e32 v[190:191], v188
	v_cvt_pk_f32_fp8_sdwa v[192:193], v188 src0_sel:WORD_1
	v_cvt_pk_f32_fp8_e32 v[194:195], v189
	v_cvt_pk_f32_fp8_sdwa v[196:197], v189 src0_sel:WORD_1
	v_cvt_pk_bf16_f32 v188, v190, v191
	v_cvt_pk_bf16_f32 v189, v192, v193
	v_cvt_pk_bf16_f32 v190, v194, v195
	v_cvt_pk_bf16_f32 v191, v196, v197
	ds_read_b64 v[192:193], v171 offset:8192
	v_mfma_f32_32x32x16_bf16 v[114:129], v[172:175], v[188:191], v[114:129]
	s_waitcnt lgkmcnt(0)
	v_cvt_pk_f32_fp8_e32 v[194:195], v192
	v_cvt_pk_f32_fp8_e32 v[196:197], v193
	v_mfma_f32_32x32x16_bf16 v[18:33], v[176:179], v[188:191], v[18:33]
	v_mfma_f32_32x32x16_bf16 v[66:81], v[180:183], v[188:191], v[66:81]
	v_mfma_f32_32x32x16_bf16 v[2:17], v[184:187], v[188:191], v[2:17]
	v_cvt_pk_f32_fp8_sdwa v[190:191], v192 src0_sel:WORD_1
	v_cvt_pk_f32_fp8_sdwa v[192:193], v193 src0_sel:WORD_1
	v_cvt_pk_bf16_f32 v188, v194, v195
	v_cvt_pk_bf16_f32 v189, v190, v191
	v_cvt_pk_bf16_f32 v190, v196, v197
	v_cvt_pk_bf16_f32 v191, v192, v193
	s_nop 0
	v_mfma_f32_32x32x16_bf16 v[82:97], v[172:175], v[188:191], v[82:97]
	v_mfma_f32_32x32x16_bf16 v[50:65], v[176:179], v[188:191], v[50:65]
	v_mfma_f32_32x32x16_bf16 v[98:113], v[180:183], v[188:191], v[98:113]
	v_mfma_f32_32x32x16_bf16 v[34:49], v[184:187], v[188:191], v[34:49]
	s_add_u32 s56, s14, s10
	s_waitcnt vmcnt(6)
	s_addc_u32 s57, s15, 0
	s_mov_b32 m0, s54
	s_waitcnt lgkmcnt(0)
	s_barrier
	v_lshl_add_u64 v[172:173], s[56:57], 0, v[146:147]
	global_load_lds_dwordx4 v[172:173], off
	v_lshl_add_u64 v[172:173], s[56:57], 0, v[158:159]
	s_add_i32 m0, s54, 0x2000
	s_addk_i32 s53, 0x402
	global_load_lds_dwordx4 v[172:173], off
	s_bfe_u32 s10, s53, 0x70009
	s_mul_i32 s10, s10, 3
	s_sub_i32 s10, s37, s10
	s_add_i32 s10, s10, 6
	s_and_b32 s10, s10, 0xff
	s_lshl_b32 s10, s10, 14
	s_add_i32 s37, s39, s10
	v_add_u32_e32 v171, s37, v160
	v_add_u32_e32 v198, v171, v163
	ds_read_b64 v[188:189], v198
	ds_read_b128 v[172:175], v154 offset:57344
	ds_read_b128 v[176:179], v154 offset:59392
	ds_read_b128 v[180:183], v154 offset:61440
	ds_read_b128 v[184:187], v154 offset:63488
	s_waitcnt lgkmcnt(0)
	v_cvt_pk_f32_fp8_e32 v[190:191], v188
	v_cvt_pk_f32_fp8_sdwa v[192:193], v188 src0_sel:WORD_1
	v_cvt_pk_f32_fp8_e32 v[194:195], v189
	v_cvt_pk_f32_fp8_sdwa v[196:197], v189 src0_sel:WORD_1
	v_cvt_pk_bf16_f32 v188, v190, v191
	v_cvt_pk_bf16_f32 v189, v192, v193
	v_cvt_pk_bf16_f32 v190, v194, v195
	v_cvt_pk_bf16_f32 v191, v196, v197
	ds_read_b64 v[192:193], v198 offset:8192
	s_waitcnt lgkmcnt(0)
	v_cvt_pk_f32_fp8_e32 v[194:195], v192
	v_cvt_pk_f32_fp8_sdwa v[196:197], v192 src0_sel:WORD_1
	v_cvt_pk_f32_fp8_e32 v[198:199], v193
	v_cvt_pk_f32_fp8_sdwa v[200:201], v193 src0_sel:WORD_1
	v_cvt_pk_bf16_f32 v192, v194, v195
	v_cvt_pk_bf16_f32 v193, v196, v197
	v_cvt_pk_bf16_f32 v194, v198, v199
	v_cvt_pk_bf16_f32 v195, v200, v201
	s_nop 1
	v_mfma_f32_32x32x16_bf16 v[114:129], v[172:175], v[188:191], v[114:129]
	v_mfma_f32_32x32x16_bf16 v[18:33], v[176:179], v[188:191], v[18:33]
	v_mfma_f32_32x32x16_bf16 v[66:81], v[180:183], v[188:191], v[66:81]
	v_mfma_f32_32x32x16_bf16 v[2:17], v[184:187], v[188:191], v[2:17]
	v_mfma_f32_32x32x16_bf16 v[82:97], v[172:175], v[192:195], v[82:97]
	v_mfma_f32_32x32x16_bf16 v[50:65], v[176:179], v[192:195], v[50:65]
	v_mfma_f32_32x32x16_bf16 v[98:113], v[180:183], v[192:195], v[98:113]
	v_mfma_f32_32x32x16_bf16 v[34:49], v[184:187], v[192:195], v[34:49]
	s_waitcnt vmcnt(6)
	s_cmp_lt_u32 s52, 60
	v_cvt_pk_bf16_f32 v138, v138, v142
	ds_write_b32 v169, v138 offset:49152
	v_cvt_pk_bf16_f32 v138, v139, v143
	s_cselect_b32 s10, s36, 0x7e0
	ds_write_b32 v169, v138 offset:49216
	v_cvt_pk_bf16_f32 v138, v140, v144
	s_lshl_b64 s[54:55], s[10:11], 11
	ds_write_b32 v169, v138 offset:49280
	v_cvt_pk_bf16_f32 v138, v141, v145
	ds_write_b32 v169, v138 offset:49344
	v_lshl_add_u64 v[142:143], v[156:157], 0, s[54:55]
	global_load_dwordx4 v[138:141], v[142:143], off sc1 nt
	v_lshl_add_u64 v[142:143], v[142:143], 0, s[22:23]
	global_load_dwordx4 v[142:145], v[142:143], off sc1 nt
	v_add_u32_e32 v154, v171, v165
	ds_read_b64 v[188:189], v154
	ds_read_b128 v[172:175], v202 offset:57344
	ds_read_b128 v[176:179], v202 offset:59392
	ds_read_b128 v[180:183], v202 offset:61440
	ds_read_b128 v[184:187], v202 offset:63488
	s_waitcnt lgkmcnt(0)
	v_cvt_pk_f32_fp8_e32 v[190:191], v188
	v_cvt_pk_f32_fp8_sdwa v[192:193], v188 src0_sel:WORD_1
	v_cvt_pk_f32_fp8_e32 v[194:195], v189
	v_cvt_pk_f32_fp8_sdwa v[196:197], v189 src0_sel:WORD_1
	v_cvt_pk_bf16_f32 v188, v190, v191
	v_cvt_pk_bf16_f32 v189, v192, v193
	v_cvt_pk_bf16_f32 v190, v194, v195
	v_cvt_pk_bf16_f32 v191, v196, v197
	ds_read_b64 v[192:193], v154 offset:8192
	v_mfma_f32_32x32x16_bf16 v[114:129], v[172:175], v[188:191], v[114:129]
	s_waitcnt lgkmcnt(0)
	v_cvt_pk_f32_fp8_e32 v[194:195], v192
	v_cvt_pk_f32_fp8_e32 v[196:197], v193
	v_mfma_f32_32x32x16_bf16 v[18:33], v[176:179], v[188:191], v[18:33]
	v_mfma_f32_32x32x16_bf16 v[66:81], v[180:183], v[188:191], v[66:81]
	v_mfma_f32_32x32x16_bf16 v[2:17], v[184:187], v[188:191], v[2:17]
	v_cvt_pk_f32_fp8_sdwa v[190:191], v192 src0_sel:WORD_1
	v_cvt_pk_f32_fp8_sdwa v[192:193], v193 src0_sel:WORD_1
	v_cvt_pk_bf16_f32 v188, v194, v195
	v_cvt_pk_bf16_f32 v189, v190, v191
	v_cvt_pk_bf16_f32 v190, v196, v197
	v_cvt_pk_bf16_f32 v191, v192, v193
	s_nop 0
	v_mfma_f32_32x32x16_bf16 v[82:97], v[172:175], v[188:191], v[82:97]
	v_mfma_f32_32x32x16_bf16 v[50:65], v[176:179], v[188:191], v[50:65]
	v_mfma_f32_32x32x16_bf16 v[98:113], v[180:183], v[188:191], v[98:113]
	v_mfma_f32_32x32x16_bf16 v[34:49], v[184:187], v[188:191], v[34:49]
	s_add_u32 s54, s14, s10
	s_waitcnt vmcnt(6)
	s_addc_u32 s55, s15, 0
	s_mov_b32 m0, s37
	s_waitcnt lgkmcnt(0)
	s_barrier
	v_lshl_add_u64 v[172:173], s[54:55], 0, v[146:147]
	global_load_lds_dwordx4 v[172:173], off
	v_lshl_add_u64 v[172:173], s[54:55], 0, v[158:159]
	s_add_i32 m0, s37, 0x2000
	s_add_i32 s36, s36, 64
	global_load_lds_dwordx4 v[172:173], off
	s_cmp_gt_u32 s52, 61
	s_mov_b32 s37, s52
	s_cbranch_scc0 .Lmoe_G2_1019
	s_branch .Lmoe_X_1019
.Lmoe_G3_1019:
	s_mul_i32 s53, s37, 0xab
	s_add_i32 s10, s53, 0x357
	s_bfe_u32 s10, s10, 0x70009
	s_mul_i32 s10, s10, 3
	s_sub_i32 s10, s37, s10
	s_add_i32 s10, s10, 5
	s_and_b32 s10, s10, 0xff
	s_lshl_b32 s10, s10, 14
	s_add_i32 s54, s39, s10
	s_add_i32 s52, s37, 2
	v_add_u32_e32 v171, s54, v160
	v_add_u32_e32 v198, v171, v163
	v_add_u32_e32 v154, v161, v162
	ds_read_b64 v[188:189], v198
	ds_read_b128 v[172:175], v154 offset:49152
	ds_read_b128 v[176:179], v154 offset:51200
	ds_read_b128 v[180:183], v154 offset:53248
	ds_read_b128 v[184:187], v154 offset:55296
	s_waitcnt lgkmcnt(0)
	v_cvt_pk_f32_fp8_e32 v[190:191], v188
	v_cvt_pk_f32_fp8_sdwa v[192:193], v188 src0_sel:WORD_1
	v_cvt_pk_f32_fp8_e32 v[194:195], v189
	v_cvt_pk_f32_fp8_sdwa v[196:197], v189 src0_sel:WORD_1
	v_cvt_pk_bf16_f32 v188, v190, v191
	v_cvt_pk_bf16_f32 v189, v192, v193
	v_cvt_pk_bf16_f32 v190, v194, v195
	v_cvt_pk_bf16_f32 v191, v196, v197
	ds_read_b64 v[192:193], v198 offset:8192
	s_waitcnt lgkmcnt(0)
	v_cvt_pk_f32_fp8_e32 v[194:195], v192
	v_cvt_pk_f32_fp8_sdwa v[196:197], v192 src0_sel:WORD_1
	v_cvt_pk_f32_fp8_e32 v[198:199], v193
	v_cvt_pk_f32_fp8_sdwa v[200:201], v193 src0_sel:WORD_1
	v_cvt_pk_bf16_f32 v192, v194, v195
	v_cvt_pk_bf16_f32 v193, v196, v197
	v_cvt_pk_bf16_f32 v194, v198, v199
	v_cvt_pk_bf16_f32 v195, v200, v201
	s_nop 1
	v_mfma_f32_32x32x16_bf16 v[114:129], v[172:175], v[188:191], v[114:129]
	v_mfma_f32_32x32x16_bf16 v[18:33], v[176:179], v[188:191], v[18:33]
	v_mfma_f32_32x32x16_bf16 v[66:81], v[180:183], v[188:191], v[66:81]
	v_mfma_f32_32x32x16_bf16 v[2:17], v[184:187], v[188:191], v[2:17]
	v_mfma_f32_32x32x16_bf16 v[82:97], v[172:175], v[192:195], v[82:97]
	v_mfma_f32_32x32x16_bf16 v[50:65], v[176:179], v[192:195], v[50:65]
	v_mfma_f32_32x32x16_bf16 v[98:113], v[180:183], v[192:195], v[98:113]
	v_mfma_f32_32x32x16_bf16 v[34:49], v[184:187], v[192:195], v[34:49]
	v_add_u32_e32 v171, v171, v165
	v_add_u32_e32 v202, v161, v164
	ds_read_b64 v[188:189], v171
	ds_read_b128 v[172:175], v202 offset:49152
	ds_read_b128 v[176:179], v202 offset:51200
	ds_read_b128 v[180:183], v202 offset:53248
	ds_read_b128 v[184:187], v202 offset:55296
	s_waitcnt lgkmcnt(0)
	v_cvt_pk_f32_fp8_e32 v[190:191], v188
	v_cvt_pk_f32_fp8_sdwa v[192:193], v188 src0_sel:WORD_1
	v_cvt_pk_f32_fp8_e32 v[194:195], v189
	v_cvt_pk_f32_fp8_sdwa v[196:197], v189 src0_sel:WORD_1
	v_cvt_pk_bf16_f32 v188, v190, v191
	v_cvt_pk_bf16_f32 v189, v192, v193
	v_cvt_pk_bf16_f32 v190, v194, v195
	v_cvt_pk_bf16_f32 v191, v196, v197
	ds_read_b64 v[192:193], v171 offset:8192
	v_mfma_f32_32x32x16_bf16 v[114:129], v[172:175], v[188:191], v[114:129]
	s_waitcnt lgkmcnt(0)
	v_cvt_pk_f32_fp8_e32 v[194:195], v192
	v_cvt_pk_f32_fp8_e32 v[196:197], v193
	v_mfma_f32_32x32x16_bf16 v[18:33], v[176:179], v[188:191], v[18:33]
	v_mfma_f32_32x32x16_bf16 v[66:81], v[180:183], v[188:191], v[66:81]
	v_mfma_f32_32x32x16_bf16 v[2:17], v[184:187], v[188:191], v[2:17]
	v_cvt_pk_f32_fp8_sdwa v[190:191], v192 src0_sel:WORD_1
	v_cvt_pk_f32_fp8_sdwa v[192:193], v193 src0_sel:WORD_1
	v_cvt_pk_bf16_f32 v188, v194, v195
	v_cvt_pk_bf16_f32 v189, v190, v191
	v_cvt_pk_bf16_f32 v190, v196, v197
	v_cvt_pk_bf16_f32 v191, v192, v193
	s_nop 0
	v_mfma_f32_32x32x16_bf16 v[82:97], v[172:175], v[188:191], v[82:97]
	v_mfma_f32_32x32x16_bf16 v[50:65], v[176:179], v[188:191], v[50:65]
	v_mfma_f32_32x32x16_bf16 v[98:113], v[180:183], v[188:191], v[98:113]
	v_mfma_f32_32x32x16_bf16 v[34:49], v[184:187], v[188:191], v[34:49]
	s_waitcnt vmcnt(6)
	s_sub_i32 s10, s36, 32
	v_cvt_pk_bf16_f32 v130, v130, v134
	s_cmp_lt_u32 s52, 61
	ds_write_b32 v169, v130 offset:57344
	v_cvt_pk_bf16_f32 v130, v131, v135
	s_cselect_b32 s10, s10, 0x7e0
	ds_write_b32 v169, v130 offset:57408
	v_cvt_pk_bf16_f32 v130, v132, v136
	s_lshl_b64 s[56:57], s[10:11], 11
	ds_write_b32 v169, v130 offset:57472
	v_cvt_pk_bf16_f32 v130, v133, v137
	ds_write_b32 v169, v130 offset:57536
	v_lshl_add_u64 v[134:135], v[156:157], 0, s[56:57]
	global_load_dwordx4 v[130:133], v[134:135], off sc1 nt
	v_lshl_add_u64 v[134:135], v[134:135], 0, s[22:23]
	global_load_dwordx4 v[134:137], v[134:135], off sc1 nt
	s_add_u32 s56, s14, s10
	s_waitcnt vmcnt(6)
	s_addc_u32 s57, s15, 0
	s_mov_b32 m0, s54
	s_waitcnt lgkmcnt(0)
	s_barrier
	v_lshl_add_u64 v[172:173], s[56:57], 0, v[146:147]
	global_load_lds_dwordx4 v[172:173], off
	v_lshl_add_u64 v[172:173], s[56:57], 0, v[158:159]
	s_add_i32 m0, s54, 0x2000
	s_addk_i32 s53, 0x402
	global_load_lds_dwordx4 v[172:173], off
	s_bfe_u32 s10, s53, 0x70009
	s_mul_i32 s10, s10, 3
	s_sub_i32 s10, s37, s10
	s_add_i32 s10, s10, 6
	s_and_b32 s10, s10, 0xff
	s_lshl_b32 s10, s10, 14
	s_add_i32 s37, s39, s10
	v_add_u32_e32 v171, s37, v160
	v_add_u32_e32 v198, v171, v163
	ds_read_b64 v[188:189], v198
	ds_read_b128 v[172:175], v154 offset:57344
	ds_read_b128 v[176:179], v154 offset:59392
	ds_read_b128 v[180:183], v154 offset:61440
	ds_read_b128 v[184:187], v154 offset:63488
	s_waitcnt lgkmcnt(0)
	v_cvt_pk_f32_fp8_e32 v[190:191], v188
	v_cvt_pk_f32_fp8_sdwa v[192:193], v188 src0_sel:WORD_1
	v_cvt_pk_f32_fp8_e32 v[194:195], v189
	v_cvt_pk_f32_fp8_sdwa v[196:197], v189 src0_sel:WORD_1
	v_cvt_pk_bf16_f32 v188, v190, v191
	v_cvt_pk_bf16_f32 v189, v192, v193
	v_cvt_pk_bf16_f32 v190, v194, v195
	v_cvt_pk_bf16_f32 v191, v196, v197
	ds_read_b64 v[192:193], v198 offset:8192
	s_waitcnt lgkmcnt(0)
	v_cvt_pk_f32_fp8_e32 v[194:195], v192
	v_cvt_pk_f32_fp8_sdwa v[196:197], v192 src0_sel:WORD_1
	v_cvt_pk_f32_fp8_e32 v[198:199], v193
	v_cvt_pk_f32_fp8_sdwa v[200:201], v193 src0_sel:WORD_1
	v_cvt_pk_bf16_f32 v192, v194, v195
	v_cvt_pk_bf16_f32 v193, v196, v197
	v_cvt_pk_bf16_f32 v194, v198, v199
	v_cvt_pk_bf16_f32 v195, v200, v201
	s_nop 1
	v_mfma_f32_32x32x16_bf16 v[114:129], v[172:175], v[188:191], v[114:129]
	v_mfma_f32_32x32x16_bf16 v[18:33], v[176:179], v[188:191], v[18:33]
	v_mfma_f32_32x32x16_bf16 v[66:81], v[180:183], v[188:191], v[66:81]
	v_mfma_f32_32x32x16_bf16 v[2:17], v[184:187], v[188:191], v[2:17]
	v_mfma_f32_32x32x16_bf16 v[82:97], v[172:175], v[192:195], v[82:97]
	v_mfma_f32_32x32x16_bf16 v[50:65], v[176:179], v[192:195], v[50:65]
	v_mfma_f32_32x32x16_bf16 v[98:113], v[180:183], v[192:195], v[98:113]
	v_mfma_f32_32x32x16_bf16 v[34:49], v[184:187], v[192:195], v[34:49]
	v_add_u32_e32 v154, v171, v165
	ds_read_b64 v[188:189], v154
	ds_read_b128 v[172:175], v202 offset:57344
	ds_read_b128 v[176:179], v202 offset:59392
	ds_read_b128 v[180:183], v202 offset:61440
	ds_read_b128 v[184:187], v202 offset:63488
	s_waitcnt lgkmcnt(0)
	v_cvt_pk_f32_fp8_e32 v[190:191], v188
	v_cvt_pk_f32_fp8_sdwa v[192:193], v188 src0_sel:WORD_1
	v_cvt_pk_f32_fp8_e32 v[194:195], v189
	v_cvt_pk_f32_fp8_sdwa v[196:197], v189 src0_sel:WORD_1
	v_cvt_pk_bf16_f32 v188, v190, v191
	v_cvt_pk_bf16_f32 v189, v192, v193
	v_cvt_pk_bf16_f32 v190, v194, v195
	v_cvt_pk_bf16_f32 v191, v196, v197
	ds_read_b64 v[192:193], v154 offset:8192
	v_mfma_f32_32x32x16_bf16 v[114:129], v[172:175], v[188:191], v[114:129]
	s_waitcnt lgkmcnt(0)
	v_cvt_pk_f32_fp8_e32 v[194:195], v192
	v_cvt_pk_f32_fp8_e32 v[196:197], v193
	v_mfma_f32_32x32x16_bf16 v[18:33], v[176:179], v[188:191], v[18:33]
	v_mfma_f32_32x32x16_bf16 v[66:81], v[180:183], v[188:191], v[66:81]
	v_mfma_f32_32x32x16_bf16 v[2:17], v[184:187], v[188:191], v[2:17]
	v_cvt_pk_f32_fp8_sdwa v[190:191], v192 src0_sel:WORD_1
	v_cvt_pk_f32_fp8_sdwa v[192:193], v193 src0_sel:WORD_1
	v_cvt_pk_bf16_f32 v188, v194, v195
	v_cvt_pk_bf16_f32 v189, v190, v191
	v_cvt_pk_bf16_f32 v190, v196, v197
	v_cvt_pk_bf16_f32 v191, v192, v193
	s_nop 0
	v_mfma_f32_32x32x16_bf16 v[82:97], v[172:175], v[188:191], v[82:97]
	v_mfma_f32_32x32x16_bf16 v[50:65], v[176:179], v[188:191], v[50:65]
	v_mfma_f32_32x32x16_bf16 v[98:113], v[180:183], v[188:191], v[98:113]
	v_mfma_f32_32x32x16_bf16 v[34:49], v[184:187], v[188:191], v[34:49]
	s_waitcnt vmcnt(6)
	s_cmp_lt_u32 s52, 60
	v_cvt_pk_bf16_f32 v138, v138, v142
	ds_write_b32 v169, v138 offset:49152
	v_cvt_pk_bf16_f32 v138, v139, v143
	s_cselect_b32 s10, s36, 0x7e0
	ds_write_b32 v169, v138 offset:49216
	v_cvt_pk_bf16_f32 v138, v140, v144
	s_lshl_b64 s[54:55], s[10:11], 11
	ds_write_b32 v169, v138 offset:49280
	v_cvt_pk_bf16_f32 v138, v141, v145
	ds_write_b32 v169, v138 offset:49344
	v_lshl_add_u64 v[142:143], v[156:157], 0, s[54:55]
	global_load_dwordx4 v[138:141], v[142:143], off sc1 nt
	v_lshl_add_u64 v[142:143], v[142:143], 0, s[22:23]
	global_load_dwordx4 v[142:145], v[142:143], off sc1 nt
	s_add_u32 s54, s14, s10
	s_waitcnt vmcnt(6)
	s_addc_u32 s55, s15, 0
	s_mov_b32 m0, s37
	s_waitcnt lgkmcnt(0)
	s_barrier
	v_lshl_add_u64 v[172:173], s[54:55], 0, v[146:147]
	global_load_lds_dwordx4 v[172:173], off
	v_lshl_add_u64 v[172:173], s[54:55], 0, v[158:159]
	s_add_i32 m0, s37, 0x2000
	s_add_i32 s36, s36, 64
	global_load_lds_dwordx4 v[172:173], off
	s_cmp_gt_u32 s52, 61
	s_mov_b32 s37, s52
	s_cbranch_scc0 .Lmoe_G3_1019

.LBB0_1084:
	s_add_i32 s31, s30, s34
	s_lshl_b32 s35, s31, 2
	s_add_i32 s35, s35, 0
	s_add_i32 s35, s35, 0x20000
	v_mov_b32_e32 v2, s35
	ds_read_b32 v2, v2
	s_waitcnt lgkmcnt(0)
	v_readfirstlane_b32 s35, v2
	s_cmp_gt_i32 s35, s10
	s_cselect_b32 s34, s34, s31
	s_lshr_b32 s31, s30, 1
	s_cmp_lt_u32 s30, 2
	s_mov_b32 s30, s31
	s_cbranch_scc0 .LBB0_1084
	s_lshl_b32 s30, s34, 2
	s_add_i32 s30, s30, 0
	s_add_i32 s30, s30, 0x20000
	v_mov_b32_e32 v4, s30
	ds_read2_b32 v[2:3], v4 offset1:80
	ds_read_b32 v4, v4 offset:640
	s_mov_b32 s35, s11
	s_waitcnt lgkmcnt(1)
	v_readfirstlane_b32 s30, v2
	s_sub_i32 s30, s10, s30
	v_readfirstlane_b32 s31, v3
	s_lshl_b32 s47, s30, 9
	s_waitcnt lgkmcnt(0)
	v_readfirstlane_b32 s49, v4
	s_sub_i32 s30, s31, s47
	s_add_i32 s49, s49, s47
	s_min_i32 s48, s30, 0x200
	s_lshl_b64 s[30:31], s[34:35], 22
	s_add_u32 s35, s6, s30
	s_addc_u32 s50, s7, s31
	s_lshl_b32 s10, s10, 11
	s_lshl_b32 s30, s46, 7
	s_sub_i32 s30, s30, s10
	s_ashr_i32 s31, s30, 31
	v_cmp_gt_i32_e32 vcc, s48, v0
	s_lshl_b64 s[36:37], s[30:31], 2
	s_add_u32 s36, s35, s36
	v_cndmask_b32_e32 v2, 0, v0, vcc
	v_add_u32_e32 v2, s49, v2
	s_addc_u32 s37, s50, s37
	v_lshl_or_b32 v146, v2, 9, v1
	v_lshl_add_u64 v[2:3], s[36:37], 0, v[152:153]
	v_lshl_add_u64 v[154:155], v[2:3], 0, v[148:149]
	s_mov_b64 s[36:37], -1
	s_cmp_ge_i32 s38, s48
	v_lshl_add_u64 v[132:133], v[154:155], 0, s[20:21]
	v_lshl_add_u64 v[130:131], v[154:155], 0, s[22:23]
	v_lshl_add_u64 v[134:135], v[154:155], 0, s[24:25]
	v_lshl_add_u64 v[138:139], v[154:155], 0, s[26:27]
	v_lshl_add_u64 v[142:143], v[154:155], 0, s[28:29]
	s_cbranch_scc0 .LBB0_1089
	global_load_dwordx4 v[2:5], v[154:155], off sc1 nt
	s_mov_b32 m0, s39
	global_load_dwordx4 v[6:9], v[132:133], off sc1 nt
	v_lshl_add_u64 v[82:83], s[12:13], 0, v[146:147]
	global_load_lds_dwordx4 v146, s[12:13]
	global_load_dwordx4 v[66:69], v[130:131], off sc1 nt
	global_load_dwordx4 v[70:73], v[134:135], off sc1 nt
	s_mov_b32 m0, s40
	s_nop 0
	global_load_lds_dwordx4 v146, s[14:15]
	s_waitcnt vmcnt(4)
	s_nop 0
	v_cvt_pk_bf16_f32 v2, v2, v6
	ds_write_b32 v167, v2 offset:49152
	v_cvt_pk_bf16_f32 v2, v3, v7
	ds_write_b32 v167, v2 offset:49216
	v_cvt_pk_bf16_f32 v2, v4, v8
	ds_write_b32 v167, v2 offset:49280
	v_cvt_pk_bf16_f32 v2, v5, v9
	ds_write_b32 v167, v2 offset:49344
	global_load_dwordx4 v[74:77], v[138:139], off sc1 nt
	global_load_dwordx4 v[78:81], v[142:143], off sc1 nt
	s_waitcnt vmcnt(5)
	s_mov_b32 m0, s41
	s_waitcnt lgkmcnt(0)
	s_barrier
	global_load_lds_dwordx4 v146, s[16:17]
	v_mov_b32_e32 v2, 0
	s_mov_b32 s36, -2
	s_movk_i32 s35, 0x80
	v_mov_b32_e32 v3, v2
	v_mov_b32_e32 v4, v2
	v_mov_b32_e32 v5, v2
	v_mov_b32_e32 v6, v2
	v_mov_b32_e32 v7, v2
	v_mov_b32_e32 v8, v2
	v_mov_b32_e32 v9, v2
	v_mov_b32_e32 v10, v2
	v_mov_b32_e32 v11, v2
	v_mov_b32_e32 v12, v2
	v_mov_b32_e32 v13, v2
	v_mov_b32_e32 v14, v2
	v_mov_b32_e32 v15, v2
	v_mov_b32_e32 v16, v2
	v_mov_b32_e32 v17, v2
	v_mov_b32_e32 v18, v2
	v_mov_b32_e32 v19, v2
	v_mov_b32_e32 v20, v2
	v_mov_b32_e32 v21, v2
	v_mov_b32_e32 v22, v2
	v_mov_b32_e32 v23, v2
	v_mov_b32_e32 v24, v2
	v_mov_b32_e32 v25, v2
	v_mov_b32_e32 v26, v2
	v_mov_b32_e32 v27, v2
	v_mov_b32_e32 v28, v2
	v_mov_b32_e32 v29, v2
	v_mov_b32_e32 v30, v2
	v_mov_b32_e32 v31, v2
	v_mov_b32_e32 v32, v2
	v_mov_b32_e32 v33, v2
	v_mov_b32_e32 v34, v2
	v_mov_b32_e32 v35, v2
	v_mov_b32_e32 v36, v2
	v_mov_b32_e32 v37, v2
	v_mov_b32_e32 v38, v2
	v_mov_b32_e32 v39, v2
	v_mov_b32_e32 v40, v2
	v_mov_b32_e32 v41, v2
	v_mov_b32_e32 v42, v2
	v_mov_b32_e32 v43, v2
	v_mov_b32_e32 v44, v2
	v_mov_b32_e32 v45, v2
	v_mov_b32_e32 v46, v2
	v_mov_b32_e32 v47, v2
	v_mov_b32_e32 v48, v2
	v_mov_b32_e32 v49, v2
	v_mov_b32_e32 v50, v2
	v_mov_b32_e32 v51, v2
	v_mov_b32_e32 v52, v2
	v_mov_b32_e32 v53, v2
	v_mov_b32_e32 v54, v2
	v_mov_b32_e32 v55, v2
	v_mov_b32_e32 v56, v2
	v_mov_b32_e32 v57, v2
	v_mov_b32_e32 v58, v2
	v_mov_b32_e32 v59, v2
	v_mov_b32_e32 v60, v2
	v_mov_b32_e32 v61, v2
	v_mov_b32_e32 v62, v2
	v_mov_b32_e32 v63, v2
	v_mov_b32_e32 v64, v2
	v_mov_b32_e32 v65, v2
	v_readfirstlane_b32 s98, v250
	s_bfe_u32 s98, s98, 0x20006
	s_cmp_eq_u32 s98, 1
	s_cbranch_scc1 .Lmoe_G1_1087
	s_cmp_eq_u32 s98, 2
	s_cbranch_scc1 .Lmoe_G2_1087
	s_cmp_eq_u32 s98, 3
	s_cbranch_scc1 .Lmoe_G3_1087
.LBB0_1087:
	s_mul_i32 s52, s36, 0xab
	s_add_i32 s10, s52, 0x357
	s_bfe_u32 s10, s10, 0x70009
	s_mul_i32 s10, s10, 3
	s_sub_i32 s10, s36, s10
	s_add_i32 s10, s10, 5
	s_and_b32 s10, s10, 0xff
	s_lshl_b32 s10, s10, 14
	s_add_i32 s53, s39, s10
	s_add_i32 s37, s36, 2
	s_waitcnt vmcnt(4)
	s_sub_i32 s10, s35, 32
	v_cvt_pk_bf16_f32 v66, v66, v70
	s_cmp_lt_u32 s37, 13
	ds_write_b32 v167, v66 offset:57344
	v_cvt_pk_bf16_f32 v66, v67, v71
	s_cselect_b32 s10, s10, 0x1e0
	ds_write_b32 v167, v66 offset:57408
	v_cvt_pk_bf16_f32 v66, v68, v72
	s_lshl_b64 s[50:51], s[10:11], 13
	ds_write_b32 v167, v66 offset:57472
	v_cvt_pk_bf16_f32 v66, v69, v73
	ds_write_b32 v167, v66 offset:57536
	v_lshl_add_u64 v[70:71], v[154:155], 0, s[50:51]
	global_load_dwordx4 v[66:69], v[70:71], off sc1 nt
	v_lshl_add_u64 v[70:71], v[70:71], 0, s[20:21]
	global_load_dwordx4 v[70:73], v[70:71], off sc1 nt
	v_add_u32_e32 v111, s53, v158
	v_add_u32_e32 v84, v111, v161
	v_add_u32_e32 v110, v159, v160
	ds_read_b64 v[100:101], v84
	ds_read_b128 v[84:87], v110 offset:49152
	ds_read_b128 v[88:91], v110 offset:51200
	ds_read_b128 v[92:95], v110 offset:53248
	ds_read_b128 v[96:99], v110 offset:55296
	s_waitcnt lgkmcnt(0)
	v_cvt_pk_f32_fp8_e32 v[102:103], v100
	v_cvt_pk_f32_fp8_sdwa v[104:105], v100 src0_sel:WORD_1
	v_cvt_pk_f32_fp8_e32 v[106:107], v101
	v_cvt_pk_f32_fp8_sdwa v[108:109], v101 src0_sel:WORD_1
	v_cvt_pk_bf16_f32 v100, v102, v103
	v_cvt_pk_bf16_f32 v101, v104, v105
	v_cvt_pk_bf16_f32 v102, v106, v107
	v_cvt_pk_bf16_f32 v103, v108, v109
	s_nop 1
	v_mfma_f32_32x32x16_bf16 v[50:65], v[84:87], v[100:103], v[50:65]
	v_mfma_f32_32x32x16_bf16 v[34:49], v[88:91], v[100:103], v[34:49]
	v_mfma_f32_32x32x16_bf16 v[18:33], v[92:95], v[100:103], v[18:33]
	v_mfma_f32_32x32x16_bf16 v[2:17], v[96:99], v[100:103], v[2:17]
	v_add_u32_e32 v84, v111, v163
	v_add_u32_e32 v112, v159, v162
	ds_read_b64 v[100:101], v84
	ds_read_b128 v[84:87], v112 offset:49152
	ds_read_b128 v[88:91], v112 offset:51200
	ds_read_b128 v[92:95], v112 offset:53248
	ds_read_b128 v[96:99], v112 offset:55296
	s_waitcnt lgkmcnt(0)
	v_cvt_pk_f32_fp8_e32 v[102:103], v100
	v_cvt_pk_f32_fp8_sdwa v[104:105], v100 src0_sel:WORD_1
	v_cvt_pk_f32_fp8_e32 v[106:107], v101
	v_cvt_pk_f32_fp8_sdwa v[108:109], v101 src0_sel:WORD_1
	v_cvt_pk_bf16_f32 v100, v102, v103
	v_cvt_pk_bf16_f32 v101, v104, v105
	v_cvt_pk_bf16_f32 v102, v106, v107
	v_cvt_pk_bf16_f32 v103, v108, v109
	s_nop 0
	v_mfma_f32_32x32x16_bf16 v[50:65], v[84:87], v[100:103], v[50:65]
	v_mfma_f32_32x32x16_bf16 v[34:49], v[88:91], v[100:103], v[34:49]
	v_mfma_f32_32x32x16_bf16 v[18:33], v[92:95], v[100:103], v[18:33]
	v_mfma_f32_32x32x16_bf16 v[2:17], v[96:99], v[100:103], v[2:17]
	s_waitcnt vmcnt(5)
	s_mov_b32 m0, s53
	s_waitcnt lgkmcnt(0)
	s_barrier
	v_lshl_add_u64 v[84:85], v[82:83], 0, s[10:11]
	global_load_lds_dwordx4 v[84:85], off
	s_addk_i32 s52, 0x402
	s_bfe_u32 s10, s52, 0x70009
	s_mul_i32 s10, s10, 3
	s_sub_i32 s10, s36, s10
	s_add_i32 s10, s10, 6
	s_and_b32 s10, s10, 0xff
	s_lshl_b32 s10, s10, 14
	s_add_i32 s36, s39, s10
	s_waitcnt vmcnt(4)
	s_cmp_lt_u32 s37, 12
	v_cvt_pk_bf16_f32 v74, v74, v78
	ds_write_b32 v167, v74 offset:49152
	v_cvt_pk_bf16_f32 v74, v75, v79
	s_cselect_b32 s10, s35, 0x1e0
	ds_write_b32 v167, v74 offset:49216
	v_cvt_pk_bf16_f32 v74, v76, v80
	s_lshl_b64 s[50:51], s[10:11], 13
	ds_write_b32 v167, v74 offset:49280
	v_cvt_pk_bf16_f32 v74, v77, v81
	ds_write_b32 v167, v74 offset:49344
	v_lshl_add_u64 v[78:79], v[154:155], 0, s[50:51]
	global_load_dwordx4 v[74:77], v[78:79], off sc1 nt
	v_lshl_add_u64 v[78:79], v[78:79], 0, s[20:21]
	global_load_dwordx4 v[78:81], v[78:79], off sc1 nt
	v_add_u32_e32 v111, s36, v158
	v_add_u32_e32 v84, v111, v161
	ds_read_b64 v[100:101], v84
	ds_read_b128 v[84:87], v110 offset:57344
	ds_read_b128 v[88:91], v110 offset:59392
	ds_read_b128 v[92:95], v110 offset:61440
	ds_read_b128 v[96:99], v110 offset:63488
	s_waitcnt lgkmcnt(0)
	v_cvt_pk_f32_fp8_e32 v[102:103], v100
	v_cvt_pk_f32_fp8_sdwa v[104:105], v100 src0_sel:WORD_1
	v_cvt_pk_f32_fp8_e32 v[106:107], v101
	v_cvt_pk_f32_fp8_sdwa v[108:109], v101 src0_sel:WORD_1
	v_cvt_pk_bf16_f32 v100, v102, v103
	v_cvt_pk_bf16_f32 v101, v104, v105
	v_cvt_pk_bf16_f32 v102, v106, v107
	v_cvt_pk_bf16_f32 v103, v108, v109
	s_nop 1
	v_mfma_f32_32x32x16_bf16 v[50:65], v[84:87], v[100:103], v[50:65]
	v_mfma_f32_32x32x16_bf16 v[34:49], v[88:91], v[100:103], v[34:49]
	v_mfma_f32_32x32x16_bf16 v[18:33], v[92:95], v[100:103], v[18:33]
	v_mfma_f32_32x32x16_bf16 v[2:17], v[96:99], v[100:103], v[2:17]
	v_add_u32_e32 v84, v111, v163
	ds_read_b64 v[100:101], v84
	ds_read_b128 v[84:87], v112 offset:57344
	ds_read_b128 v[88:91], v112 offset:59392
	ds_read_b128 v[92:95], v112 offset:61440
	ds_read_b128 v[96:99], v112 offset:63488
	s_waitcnt lgkmcnt(0)
	v_cvt_pk_f32_fp8_e32 v[102:103], v100
	v_cvt_pk_f32_fp8_sdwa v[104:105], v100 src0_sel:WORD_1
	v_cvt_pk_f32_fp8_e32 v[106:107], v101
	v_cvt_pk_f32_fp8_sdwa v[108:109], v101 src0_sel:WORD_1
	v_cvt_pk_bf16_f32 v100, v102, v103
	v_cvt_pk_bf16_f32 v101, v104, v105
	v_cvt_pk_bf16_f32 v102, v106, v107
	v_cvt_pk_bf16_f32 v103, v108, v109
	s_nop 0
	v_mfma_f32_32x32x16_bf16 v[50:65], v[84:87], v[100:103], v[50:65]
	v_mfma_f32_32x32x16_bf16 v[34:49], v[88:91], v[100:103], v[34:49]
	v_mfma_f32_32x32x16_bf16 v[18:33], v[92:95], v[100:103], v[18:33]
	v_mfma_f32_32x32x16_bf16 v[2:17], v[96:99], v[100:103], v[2:17]
	s_waitcnt vmcnt(5)
	s_mov_b32 m0, s36
	s_waitcnt lgkmcnt(0)
	s_barrier
	v_lshl_add_u64 v[84:85], v[82:83], 0, s[10:11]
	global_load_lds_dwordx4 v[84:85], off
	s_add_i32 s35, s35, 64
	s_cmp_gt_u32 s37, 13
	s_mov_b32 s36, s37
	s_cbranch_scc0 .LBB0_1087
	s_branch .Lmoe_X_1087

.Lmoe_G2_1087:
	s_mul_i32 s52, s36, 0xab
	s_add_i32 s10, s52, 0x357
	s_bfe_u32 s10, s10, 0x70009
	s_mul_i32 s10, s10, 3
	s_sub_i32 s10, s36, s10
	s_add_i32 s10, s10, 5
	s_and_b32 s10, s10, 0xff
	s_lshl_b32 s10, s10, 14
	s_add_i32 s53, s39, s10
	s_add_i32 s37, s36, 2
	v_add_u32_e32 v111, s53, v158
	v_add_u32_e32 v84, v111, v161
	v_add_u32_e32 v110, v159, v160
	ds_read_b64 v[100:101], v84
	ds_read_b128 v[84:87], v110 offset:49152
	ds_read_b128 v[88:91], v110 offset:51200
	ds_read_b128 v[92:95], v110 offset:53248
	ds_read_b128 v[96:99], v110 offset:55296
	s_waitcnt lgkmcnt(0)
	v_cvt_pk_f32_fp8_e32 v[102:103], v100
	v_cvt_pk_f32_fp8_sdwa v[104:105], v100 src0_sel:WORD_1
	v_cvt_pk_f32_fp8_e32 v[106:107], v101
	v_cvt_pk_f32_fp8_sdwa v[108:109], v101 src0_sel:WORD_1
	v_cvt_pk_bf16_f32 v100, v102, v103
	v_cvt_pk_bf16_f32 v101, v104, v105
	v_cvt_pk_bf16_f32 v102, v106, v107
	v_cvt_pk_bf16_f32 v103, v108, v109
	s_nop 1
	v_mfma_f32_32x32x16_bf16 v[50:65], v[84:87], v[100:103], v[50:65]
	v_mfma_f32_32x32x16_bf16 v[34:49], v[88:91], v[100:103], v[34:49]
	v_mfma_f32_32x32x16_bf16 v[18:33], v[92:95], v[100:103], v[18:33]
	v_mfma_f32_32x32x16_bf16 v[2:17], v[96:99], v[100:103], v[2:17]
	s_waitcnt vmcnt(4)
	s_sub_i32 s10, s35, 32
	v_cvt_pk_bf16_f32 v66, v66, v70
	s_cmp_lt_u32 s37, 13
	ds_write_b32 v167, v66 offset:57344
	v_cvt_pk_bf16_f32 v66, v67, v71
	s_cselect_b32 s10, s10, 0x1e0
	ds_write_b32 v167, v66 offset:57408
	v_cvt_pk_bf16_f32 v66, v68, v72
	s_lshl_b64 s[50:51], s[10:11], 13
	ds_write_b32 v167, v66 offset:57472
	v_cvt_pk_bf16_f32 v66, v69, v73
	ds_write_b32 v167, v66 offset:57536
	v_lshl_add_u64 v[70:71], v[154:155], 0, s[50:51]
	global_load_dwordx4 v[66:69], v[70:71], off sc1 nt
	v_lshl_add_u64 v[70:71], v[70:71], 0, s[20:21]
	global_load_dwordx4 v[70:73], v[70:71], off sc1 nt
	v_add_u32_e32 v84, v111, v163
	v_add_u32_e32 v112, v159, v162
	ds_read_b64 v[100:101], v84
	ds_read_b128 v[84:87], v112 offset:49152
	ds_read_b128 v[88:91], v112 offset:51200
	ds_read_b128 v[92:95], v112 offset:53248
	ds_read_b128 v[96:99], v112 offset:55296
	s_waitcnt lgkmcnt(0)
	v_cvt_pk_f32_fp8_e32 v[102:103], v100
	v_cvt_pk_f32_fp8_sdwa v[104:105], v100 src0_sel:WORD_1
	v_cvt_pk_f32_fp8_e32 v[106:107], v101
	v_cvt_pk_f32_fp8_sdwa v[108:109], v101 src0_sel:WORD_1
	v_cvt_pk_bf16_f32 v100, v102, v103
	v_cvt_pk_bf16_f32 v101, v104, v105
	v_cvt_pk_bf16_f32 v102, v106, v107
	v_cvt_pk_bf16_f32 v103, v108, v109
	s_nop 0
	v_mfma_f32_32x32x16_bf16 v[50:65], v[84:87], v[100:103], v[50:65]
	v_mfma_f32_32x32x16_bf16 v[34:49], v[88:91], v[100:103], v[34:49]
	v_mfma_f32_32x32x16_bf16 v[18:33], v[92:95], v[100:103], v[18:33]
	v_mfma_f32_32x32x16_bf16 v[2:17], v[96:99], v[100:103], v[2:17]
	s_waitcnt vmcnt(5)
	s_mov_b32 m0, s53
	s_waitcnt lgkmcnt(0)
	s_barrier
	v_lshl_add_u64 v[84:85], v[82:83], 0, s[10:11]
	global_load_lds_dwordx4 v[84:85], off
	s_addk_i32 s52, 0x402
	s_bfe_u32 s10, s52, 0x70009
	s_mul_i32 s10, s10, 3
	s_sub_i32 s10, s36, s10
	s_add_i32 s10, s10, 6
	s_and_b32 s10, s10, 0xff
	s_lshl_b32 s10, s10, 14
	s_add_i32 s36, s39, s10
	v_add_u32_e32 v111, s36, v158
	v_add_u32_e32 v84, v111, v161
	ds_read_b64 v[100:101], v84
	ds_read_b128 v[84:87], v110 offset:57344
	ds_read_b128 v[88:91], v110 offset:59392
	ds_read_b128 v[92:95], v110 offset:61440
	ds_read_b128 v[96:99], v110 offset:63488
	s_waitcnt lgkmcnt(0)
	v_cvt_pk_f32_fp8_e32 v[102:103], v100
	v_cvt_pk_f32_fp8_sdwa v[104:105], v100 src0_sel:WORD_1
	v_cvt_pk_f32_fp8_e32 v[106:107], v101
	v_cvt_pk_f32_fp8_sdwa v[108:109], v101 src0_sel:WORD_1
	v_cvt_pk_bf16_f32 v100, v102, v103
	v_cvt_pk_bf16_f32 v101, v104, v105
	v_cvt_pk_bf16_f32 v102, v106, v107
	v_cvt_pk_bf16_f32 v103, v108, v109
	s_nop 1
	v_mfma_f32_32x32x16_bf16 v[50:65], v[84:87], v[100:103], v[50:65]
	v_mfma_f32_32x32x16_bf16 v[34:49], v[88:91], v[100:103], v[34:49]
	v_mfma_f32_32x32x16_bf16 v[18:33], v[92:95], v[100:103], v[18:33]
	v_mfma_f32_32x32x16_bf16 v[2:17], v[96:99], v[100:103], v[2:17]
	s_waitcnt vmcnt(4)
	s_cmp_lt_u32 s37, 12
	v_cvt_pk_bf16_f32 v74, v74, v78
	ds_write_b32 v167, v74 offset:49152
	v_cvt_pk_bf16_f32 v74, v75, v79
	s_cselect_b32 s10, s35, 0x1e0
	ds_write_b32 v167, v74 offset:49216
	v_cvt_pk_bf16_f32 v74, v76, v80
	s_lshl_b64 s[50:51], s[10:11], 13
	ds_write_b32 v167, v74 offset:49280
	v_cvt_pk_bf16_f32 v74, v77, v81
	ds_write_b32 v167, v74 offset:49344
	v_lshl_add_u64 v[78:79], v[154:155], 0, s[50:51]
	global_load_dwordx4 v[74:77], v[78:79], off sc1 nt
	v_lshl_add_u64 v[78:79], v[78:79], 0, s[20:21]
	global_load_dwordx4 v[78:81], v[78:79], off sc1 nt
	v_add_u32_e32 v84, v111, v163
	ds_read_b64 v[100:101], v84
	ds_read_b128 v[84:87], v112 offset:57344
	ds_read_b128 v[88:91], v112 offset:59392
	ds_read_b128 v[92:95], v112 offset:61440
	ds_read_b128 v[96:99], v112 offset:63488
	s_waitcnt lgkmcnt(0)
	v_cvt_pk_f32_fp8_e32 v[102:103], v100
	v_cvt_pk_f32_fp8_sdwa v[104:105], v100 src0_sel:WORD_1
	v_cvt_pk_f32_fp8_e32 v[106:107], v101
	v_cvt_pk_f32_fp8_sdwa v[108:109], v101 src0_sel:WORD_1
	v_cvt_pk_bf16_f32 v100, v102, v103
	v_cvt_pk_bf16_f32 v101, v104, v105
	v_cvt_pk_bf16_f32 v102, v106, v107
	v_cvt_pk_bf16_f32 v103, v108, v109
	s_nop 0
	v_mfma_f32_32x32x16_bf16 v[50:65], v[84:87], v[100:103], v[50:65]
	v_mfma_f32_32x32x16_bf16 v[34:49], v[88:91], v[100:103], v[34:49]
	v_mfma_f32_32x32x16_bf16 v[18:33], v[92:95], v[100:103], v[18:33]
	v_mfma_f32_32x32x16_bf16 v[2:17], v[96:99], v[100:103], v[2:17]
	s_waitcnt vmcnt(5)
	s_mov_b32 m0, s36
	s_waitcnt lgkmcnt(0)
	s_barrier
	v_lshl_add_u64 v[84:85], v[82:83], 0, s[10:11]
	global_load_lds_dwordx4 v[84:85], off
	s_add_i32 s35, s35, 64
	s_cmp_gt_u32 s37, 13
	s_mov_b32 s36, s37
	s_cbranch_scc0 .Lmoe_G2_1087
	s_branch .Lmoe_X_1087
.Lmoe_G3_1087:
	s_mul_i32 s52, s36, 0xab
	s_add_i32 s10, s52, 0x357
	s_bfe_u32 s10, s10, 0x70009
	s_mul_i32 s10, s10, 3
	s_sub_i32 s10, s36, s10
	s_add_i32 s10, s10, 5
	s_and_b32 s10, s10, 0xff
	s_lshl_b32 s10, s10, 14
	s_add_i32 s53, s39, s10
	s_add_i32 s37, s36, 2
	v_add_u32_e32 v111, s53, v158
	v_add_u32_e32 v84, v111, v161
	v_add_u32_e32 v110, v159, v160
	ds_read_b64 v[100:101], v84
	ds_read_b128 v[84:87], v110 offset:49152
	ds_read_b128 v[88:91], v110 offset:51200
	ds_read_b128 v[92:95], v110 offset:53248
	ds_read_b128 v[96:99], v110 offset:55296
	s_waitcnt lgkmcnt(0)
	v_cvt_pk_f32_fp8_e32 v[102:103], v100
	v_cvt_pk_f32_fp8_sdwa v[104:105], v100 src0_sel:WORD_1
	v_cvt_pk_f32_fp8_e32 v[106:107], v101
	v_cvt_pk_f32_fp8_sdwa v[108:109], v101 src0_sel:WORD_1
	v_cvt_pk_bf16_f32 v100, v102, v103
	v_cvt_pk_bf16_f32 v101, v104, v105
	v_cvt_pk_bf16_f32 v102, v106, v107
	v_cvt_pk_bf16_f32 v103, v108, v109
	s_nop 1
	v_mfma_f32_32x32x16_bf16 v[50:65], v[84:87], v[100:103], v[50:65]
	v_mfma_f32_32x32x16_bf16 v[34:49], v[88:91], v[100:103], v[34:49]
	v_mfma_f32_32x32x16_bf16 v[18:33], v[92:95], v[100:103], v[18:33]
	v_mfma_f32_32x32x16_bf16 v[2:17], v[96:99], v[100:103], v[2:17]
	v_add_u32_e32 v84, v111, v163
	v_add_u32_e32 v112, v159, v162
	ds_read_b64 v[100:101], v84
	ds_read_b128 v[84:87], v112 offset:49152
	ds_read_b128 v[88:91], v112 offset:51200
	ds_read_b128 v[92:95], v112 offset:53248
	ds_read_b128 v[96:99], v112 offset:55296
	s_waitcnt lgkmcnt(0)
	v_cvt_pk_f32_fp8_e32 v[102:103], v100
	v_cvt_pk_f32_fp8_sdwa v[104:105], v100 src0_sel:WORD_1
	v_cvt_pk_f32_fp8_e32 v[106:107], v101
	v_cvt_pk_f32_fp8_sdwa v[108:109], v101 src0_sel:WORD_1
	v_cvt_pk_bf16_f32 v100, v102, v103
	v_cvt_pk_bf16_f32 v101, v104, v105
	v_cvt_pk_bf16_f32 v102, v106, v107
	v_cvt_pk_bf16_f32 v103, v108, v109
	s_nop 0
	v_mfma_f32_32x32x16_bf16 v[50:65], v[84:87], v[100:103], v[50:65]
	v_mfma_f32_32x32x16_bf16 v[34:49], v[88:91], v[100:103], v[34:49]
	v_mfma_f32_32x32x16_bf16 v[18:33], v[92:95], v[100:103], v[18:33]
	v_mfma_f32_32x32x16_bf16 v[2:17], v[96:99], v[100:103], v[2:17]
	s_waitcnt vmcnt(4)
	s_sub_i32 s10, s35, 32
	v_cvt_pk_bf16_f32 v66, v66, v70
	s_cmp_lt_u32 s37, 13
	ds_write_b32 v167, v66 offset:57344
	v_cvt_pk_bf16_f32 v66, v67, v71
	s_cselect_b32 s10, s10, 0x1e0
	ds_write_b32 v167, v66 offset:57408
	v_cvt_pk_bf16_f32 v66, v68, v72
	s_lshl_b64 s[50:51], s[10:11], 13
	ds_write_b32 v167, v66 offset:57472
	v_cvt_pk_bf16_f32 v66, v69, v73
	ds_write_b32 v167, v66 offset:57536
	v_lshl_add_u64 v[70:71], v[154:155], 0, s[50:51]
	global_load_dwordx4 v[66:69], v[70:71], off sc1 nt
	v_lshl_add_u64 v[70:71], v[70:71], 0, s[20:21]
	global_load_dwordx4 v[70:73], v[70:71], off sc1 nt
	s_waitcnt vmcnt(5)
	s_mov_b32 m0, s53
	s_waitcnt lgkmcnt(0)
	s_barrier
	v_lshl_add_u64 v[84:85], v[82:83], 0, s[10:11]
	global_load_lds_dwordx4 v[84:85], off
	s_addk_i32 s52, 0x402
	s_bfe_u32 s10, s52, 0x70009
	s_mul_i32 s10, s10, 3
	s_sub_i32 s10, s36, s10
	s_add_i32 s10, s10, 6
	s_and_b32 s10, s10, 0xff
	s_lshl_b32 s10, s10, 14
	s_add_i32 s36, s39, s10
	v_add_u32_e32 v111, s36, v158
	v_add_u32_e32 v84, v111, v161
	ds_read_b64 v[100:101], v84
	ds_read_b128 v[84:87], v110 offset:57344
	ds_read_b128 v[88:91], v110 offset:59392
	ds_read_b128 v[92:95], v110 offset:61440
	ds_read_b128 v[96:99], v110 offset:63488
	s_waitcnt lgkmcnt(0)
	v_cvt_pk_f32_fp8_e32 v[102:103], v100
	v_cvt_pk_f32_fp8_sdwa v[104:105], v100 src0_sel:WORD_1
	v_cvt_pk_f32_fp8_e32 v[106:107], v101
	v_cvt_pk_f32_fp8_sdwa v[108:109], v101 src0_sel:WORD_1
	v_cvt_pk_bf16_f32 v100, v102, v103
	v_cvt_pk_bf16_f32 v101, v104, v105
	v_cvt_pk_bf16_f32 v102, v106, v107
	v_cvt_pk_bf16_f32 v103, v108, v109
	s_nop 1
	v_mfma_f32_32x32x16_bf16 v[50:65], v[84:87], v[100:103], v[50:65]
	v_mfma_f32_32x32x16_bf16 v[34:49], v[88:91], v[100:103], v[34:49]
	v_mfma_f32_32x32x16_bf16 v[18:33], v[92:95], v[100:103], v[18:33]
	v_mfma_f32_32x32x16_bf16 v[2:17], v[96:99], v[100:103], v[2:17]
	v_add_u32_e32 v84, v111, v163
	ds_read_b64 v[100:101], v84
	ds_read_b128 v[84:87], v112 offset:57344
	ds_read_b128 v[88:91], v112 offset:59392
	ds_read_b128 v[92:95], v112 offset:61440
	ds_read_b128 v[96:99], v112 offset:63488
	s_waitcnt lgkmcnt(0)
	v_cvt_pk_f32_fp8_e32 v[102:103], v100
	v_cvt_pk_f32_fp8_sdwa v[104:105], v100 src0_sel:WORD_1
	v_cvt_pk_f32_fp8_e32 v[106:107], v101
	v_cvt_pk_f32_fp8_sdwa v[108:109], v101 src0_sel:WORD_1
	v_cvt_pk_bf16_f32 v100, v102, v103
	v_cvt_pk_bf16_f32 v101, v104, v105
	v_cvt_pk_bf16_f32 v102, v106, v107
	v_cvt_pk_bf16_f32 v103, v108, v109
	s_nop 0
	v_mfma_f32_32x32x16_bf16 v[50:65], v[84:87], v[100:103], v[50:65]
	v_mfma_f32_32x32x16_bf16 v[34:49], v[88:91], v[100:103], v[34:49]
	v_mfma_f32_32x32x16_bf16 v[18:33], v[92:95], v[100:103], v[18:33]
	v_mfma_f32_32x32x16_bf16 v[2:17], v[96:99], v[100:103], v[2:17]
	s_waitcnt vmcnt(4)
	s_cmp_lt_u32 s37, 12
	v_cvt_pk_bf16_f32 v74, v74, v78
	ds_write_b32 v167, v74 offset:49152
	v_cvt_pk_bf16_f32 v74, v75, v79
	s_cselect_b32 s10, s35, 0x1e0
	ds_write_b32 v167, v74 offset:49216
	v_cvt_pk_bf16_f32 v74, v76, v80
	s_lshl_b64 s[50:51], s[10:11], 13
	ds_write_b32 v167, v74 offset:49280
	v_cvt_pk_bf16_f32 v74, v77, v81
	ds_write_b32 v167, v74 offset:49344
	v_lshl_add_u64 v[78:79], v[154:155], 0, s[50:51]
	global_load_dwordx4 v[74:77], v[78:79], off sc1 nt
	v_lshl_add_u64 v[78:79], v[78:79], 0, s[20:21]
	global_load_dwordx4 v[78:81], v[78:79], off sc1 nt
	s_waitcnt vmcnt(5)
	s_mov_b32 m0, s36
	s_waitcnt lgkmcnt(0)
	s_barrier
	v_lshl_add_u64 v[84:85], v[82:83], 0, s[10:11]
	global_load_lds_dwordx4 v[84:85], off
	s_add_i32 s35, s35, 64
	s_cmp_gt_u32 s37, 13
	s_mov_b32 s36, s37
	s_cbranch_scc0 .Lmoe_G3_1087

.LBB0_1089:
	v_mov_b32_e32 v129, 0
	s_and_b64 vcc, exec, s[36:37]
	v_mov_b32_e32 v128, v129
	v_mov_b32_e32 v127, v129
	v_mov_b32_e32 v126, v129
	v_mov_b32_e32 v125, v129
	v_mov_b32_e32 v124, v129
	v_mov_b32_e32 v123, v129
	v_mov_b32_e32 v122, v129
	v_mov_b32_e32 v121, v129
	v_mov_b32_e32 v120, v129
	v_mov_b32_e32 v119, v129
	v_mov_b32_e32 v118, v129
	v_mov_b32_e32 v117, v129
	v_mov_b32_e32 v116, v129
	v_mov_b32_e32 v115, v129
	v_mov_b32_e32 v114, v129
	v_mov_b32_e32 v113, v129
	v_mov_b32_e32 v112, v129
	v_mov_b32_e32 v111, v129
	v_mov_b32_e32 v110, v129
	v_mov_b32_e32 v109, v129
	v_mov_b32_e32 v108, v129
	v_mov_b32_e32 v107, v129
	v_mov_b32_e32 v106, v129
	v_mov_b32_e32 v105, v129
	v_mov_b32_e32 v104, v129
	v_mov_b32_e32 v103, v129
	v_mov_b32_e32 v102, v129
	v_mov_b32_e32 v101, v129
	v_mov_b32_e32 v100, v129
	v_mov_b32_e32 v99, v129
	v_mov_b32_e32 v98, v129
	v_mov_b32_e32 v97, v129
	v_mov_b32_e32 v96, v129
	v_mov_b32_e32 v95, v129
	v_mov_b32_e32 v94, v129
	v_mov_b32_e32 v93, v129
	v_mov_b32_e32 v92, v129
	v_mov_b32_e32 v91, v129
	v_mov_b32_e32 v90, v129
	v_mov_b32_e32 v89, v129
	v_mov_b32_e32 v88, v129
	v_mov_b32_e32 v87, v129
	v_mov_b32_e32 v86, v129
	v_mov_b32_e32 v85, v129
	v_mov_b32_e32 v84, v129
	v_mov_b32_e32 v83, v129
	v_mov_b32_e32 v82, v129
	v_mov_b32_e32 v81, v129
	v_mov_b32_e32 v80, v129
	v_mov_b32_e32 v79, v129
	v_mov_b32_e32 v78, v129
	v_mov_b32_e32 v77, v129
	v_mov_b32_e32 v76, v129
	v_mov_b32_e32 v75, v129
	v_mov_b32_e32 v74, v129
	v_mov_b32_e32 v73, v129
	v_mov_b32_e32 v72, v129
	v_mov_b32_e32 v71, v129
	v_mov_b32_e32 v70, v129
	v_mov_b32_e32 v69, v129
	v_mov_b32_e32 v68, v129
	v_mov_b32_e32 v67, v129
	v_mov_b32_e32 v66, v129
	s_cbranch_vccz .LBB0_1093
	v_cmp_gt_i32_e32 vcc, s48, v165
	s_mov_b32 m0, s39
	v_mov_b32_e32 v157, v147
	v_cndmask_b32_e32 v2, 0, v165, vcc
	v_add_u32_e32 v2, s49, v2
	v_lshl_or_b32 v156, v2, 9, v1
	global_load_dwordx4 v[2:5], v[154:155], off sc1 nt
	global_load_dwordx4 v[6:9], v[132:133], off sc1 nt
	global_load_lds_dwordx4 v146, s[12:13]
	s_mov_b32 m0, s42
	s_nop 0
	global_load_lds_dwordx4 v156, s[12:13]
	global_load_dwordx4 v[130:133], v[130:131], off sc1 nt
	global_load_dwordx4 v[134:137], v[134:135], off sc1 nt
	s_mov_b32 m0, s40
	s_nop 0
	global_load_lds_dwordx4 v146, s[14:15]
	s_mov_b32 m0, s43
	s_nop 0
	global_load_lds_dwordx4 v156, s[14:15]
	s_waitcnt vmcnt(6)
	s_nop 0
	v_cvt_pk_bf16_f32 v2, v2, v6
	ds_write_b32 v167, v2 offset:49152
	v_cvt_pk_bf16_f32 v2, v3, v7
	ds_write_b32 v167, v2 offset:49216
	v_cvt_pk_bf16_f32 v2, v4, v8
	ds_write_b32 v167, v2 offset:49280
	v_cvt_pk_bf16_f32 v2, v5, v9
	ds_write_b32 v167, v2 offset:49344
	global_load_dwordx4 v[138:141], v[138:139], off sc1 nt
	global_load_dwordx4 v[142:145], v[142:143], off sc1 nt
	s_waitcnt vmcnt(6)
	s_mov_b32 m0, s41
	s_waitcnt lgkmcnt(0)
	s_barrier
	global_load_lds_dwordx4 v146, s[16:17]
	s_mov_b32 m0, s44
	v_mov_b32_e32 v66, 0
	global_load_lds_dwordx4 v156, s[16:17]
	s_mov_b32 s36, -2
	s_movk_i32 s35, 0x80
	v_mov_b32_e32 v67, v66
	v_mov_b32_e32 v68, v66
	v_mov_b32_e32 v69, v66
	v_mov_b32_e32 v70, v66
	v_mov_b32_e32 v71, v66
	v_mov_b32_e32 v72, v66
	v_mov_b32_e32 v73, v66
	v_mov_b32_e32 v74, v66
	v_mov_b32_e32 v75, v66
	v_mov_b32_e32 v76, v66
	v_mov_b32_e32 v77, v66
	v_mov_b32_e32 v78, v66
	v_mov_b32_e32 v79, v66
	v_mov_b32_e32 v80, v66
	v_mov_b32_e32 v81, v66
	v_mov_b32_e32 v82, v66
	v_mov_b32_e32 v83, v66
	v_mov_b32_e32 v84, v66
	v_mov_b32_e32 v85, v66
	v_mov_b32_e32 v86, v66
	v_mov_b32_e32 v87, v66
	v_mov_b32_e32 v88, v66
	v_mov_b32_e32 v89, v66
	v_mov_b32_e32 v90, v66
	v_mov_b32_e32 v91, v66
	v_mov_b32_e32 v92, v66
	v_mov_b32_e32 v93, v66
	v_mov_b32_e32 v94, v66
	v_mov_b32_e32 v95, v66
	v_mov_b32_e32 v96, v66
	v_mov_b32_e32 v97, v66
	v_mov_b32_e32 v98, v66
	v_mov_b32_e32 v99, v66
	v_mov_b32_e32 v100, v66
	v_mov_b32_e32 v101, v66
	v_mov_b32_e32 v102, v66
	v_mov_b32_e32 v103, v66
	v_mov_b32_e32 v104, v66
	v_mov_b32_e32 v105, v66
	v_mov_b32_e32 v106, v66
	v_mov_b32_e32 v107, v66
	v_mov_b32_e32 v108, v66
	v_mov_b32_e32 v109, v66
	v_mov_b32_e32 v110, v66
	v_mov_b32_e32 v111, v66
	v_mov_b32_e32 v112, v66
	v_mov_b32_e32 v113, v66
	v_mov_b32_e32 v114, v66
	v_mov_b32_e32 v115, v66
	v_mov_b32_e32 v116, v66
	v_mov_b32_e32 v117, v66
	v_mov_b32_e32 v118, v66
	v_mov_b32_e32 v119, v66
	v_mov_b32_e32 v120, v66
	v_mov_b32_e32 v121, v66
	v_mov_b32_e32 v122, v66
	v_mov_b32_e32 v123, v66
	v_mov_b32_e32 v124, v66
	v_mov_b32_e32 v125, v66
	v_mov_b32_e32 v126, v66
	v_mov_b32_e32 v127, v66
	v_mov_b32_e32 v128, v66
	v_mov_b32_e32 v129, v66
	v_mov_b32_e32 v2, v66
	v_mov_b32_e32 v3, v66
	v_mov_b32_e32 v4, v66
	v_mov_b32_e32 v5, v66
	v_mov_b32_e32 v6, v66
	v_mov_b32_e32 v7, v66
	v_mov_b32_e32 v8, v66
	v_mov_b32_e32 v9, v66
	v_mov_b32_e32 v10, v66
	v_mov_b32_e32 v11, v66
	v_mov_b32_e32 v12, v66
	v_mov_b32_e32 v13, v66
	v_mov_b32_e32 v14, v66
	v_mov_b32_e32 v15, v66
	v_mov_b32_e32 v16, v66
	v_mov_b32_e32 v17, v66
	v_mov_b32_e32 v18, v66
	v_mov_b32_e32 v19, v66
	v_mov_b32_e32 v20, v66
	v_mov_b32_e32 v21, v66
	v_mov_b32_e32 v22, v66
	v_mov_b32_e32 v23, v66
	v_mov_b32_e32 v24, v66
	v_mov_b32_e32 v25, v66
	v_mov_b32_e32 v26, v66
	v_mov_b32_e32 v27, v66
	v_mov_b32_e32 v28, v66
	v_mov_b32_e32 v29, v66
	v_mov_b32_e32 v30, v66
	v_mov_b32_e32 v31, v66
	v_mov_b32_e32 v32, v66
	v_mov_b32_e32 v33, v66
	v_mov_b32_e32 v34, v66
	v_mov_b32_e32 v35, v66
	v_mov_b32_e32 v36, v66
	v_mov_b32_e32 v37, v66
	v_mov_b32_e32 v38, v66
	v_mov_b32_e32 v39, v66
	v_mov_b32_e32 v40, v66
	v_mov_b32_e32 v41, v66
	v_mov_b32_e32 v42, v66
	v_mov_b32_e32 v43, v66
	v_mov_b32_e32 v44, v66
	v_mov_b32_e32 v45, v66
	v_mov_b32_e32 v46, v66
	v_mov_b32_e32 v47, v66
	v_mov_b32_e32 v48, v66
	v_mov_b32_e32 v49, v66
	v_mov_b32_e32 v50, v66
	v_mov_b32_e32 v51, v66
	v_mov_b32_e32 v52, v66
	v_mov_b32_e32 v53, v66
	v_mov_b32_e32 v54, v66
	v_mov_b32_e32 v55, v66
	v_mov_b32_e32 v56, v66
	v_mov_b32_e32 v57, v66
	v_mov_b32_e32 v58, v66
	v_mov_b32_e32 v59, v66
	v_mov_b32_e32 v60, v66
	v_mov_b32_e32 v61, v66
	v_mov_b32_e32 v62, v66
	v_mov_b32_e32 v63, v66
	v_mov_b32_e32 v64, v66
	v_mov_b32_e32 v65, v66
	v_readfirstlane_b32 s98, v250
	s_bfe_u32 s98, s98, 0x20006
	s_cmp_eq_u32 s98, 1
	s_cbranch_scc1 .Lmoe_G1_1091
	s_cmp_eq_u32 s98, 2
	s_cbranch_scc1 .Lmoe_G2_1091
	s_cmp_eq_u32 s98, 3
	s_cbranch_scc1 .Lmoe_G3_1091
.LBB0_1091:
	s_mul_i32 s49, s36, 0xab
	s_add_i32 s10, s49, 0x357
	s_bfe_u32 s10, s10, 0x70009
	s_mul_i32 s10, s10, 3
	s_sub_i32 s10, s36, s10
	s_add_i32 s10, s10, 5
	s_and_b32 s10, s10, 0xff
	s_lshl_b32 s10, s10, 14
	s_add_i32 s50, s39, s10
	s_add_i32 s37, s36, 2
	s_waitcnt vmcnt(6)
	s_sub_i32 s10, s35, 32
	v_cvt_pk_bf16_f32 v130, v130, v134
	s_cmp_lt_u32 s37, 13
	ds_write_b32 v167, v130 offset:57344
	v_cvt_pk_bf16_f32 v130, v131, v135
	s_cselect_b32 s10, s10, 0x1e0
	ds_write_b32 v167, v130 offset:57408
	v_cvt_pk_bf16_f32 v130, v132, v136
	s_lshl_b64 s[52:53], s[10:11], 13
	ds_write_b32 v167, v130 offset:57472
	v_cvt_pk_bf16_f32 v130, v133, v137
	ds_write_b32 v167, v130 offset:57536
	v_lshl_add_u64 v[134:135], v[154:155], 0, s[52:53]
	global_load_dwordx4 v[130:133], v[134:135], off sc1 nt
	v_lshl_add_u64 v[134:135], v[134:135], 0, s[20:21]
	global_load_dwordx4 v[134:137], v[134:135], off sc1 nt
	v_add_u32_e32 v200, s50, v158
	v_add_u32_e32 v196, v200, v161
	v_add_u32_e32 v169, v159, v160
	ds_read_b64 v[186:187], v196
	ds_read_b128 v[170:173], v169 offset:49152
	ds_read_b128 v[174:177], v169 offset:51200
	ds_read_b128 v[178:181], v169 offset:53248
	ds_read_b128 v[182:185], v169 offset:55296
	s_waitcnt lgkmcnt(0)
	v_cvt_pk_f32_fp8_e32 v[188:189], v186
	v_cvt_pk_f32_fp8_sdwa v[190:191], v186 src0_sel:WORD_1
	v_cvt_pk_f32_fp8_e32 v[192:193], v187
	v_cvt_pk_f32_fp8_sdwa v[194:195], v187 src0_sel:WORD_1
	v_cvt_pk_bf16_f32 v186, v188, v189
	v_cvt_pk_bf16_f32 v187, v190, v191
	v_cvt_pk_bf16_f32 v188, v192, v193
	v_cvt_pk_bf16_f32 v189, v194, v195
	ds_read_b64 v[190:191], v196 offset:8192
	s_waitcnt lgkmcnt(0)
	v_cvt_pk_f32_fp8_e32 v[192:193], v190
	v_cvt_pk_f32_fp8_sdwa v[194:195], v190 src0_sel:WORD_1
	v_cvt_pk_f32_fp8_e32 v[196:197], v191
	v_cvt_pk_f32_fp8_sdwa v[198:199], v191 src0_sel:WORD_1
	v_cvt_pk_bf16_f32 v190, v192, v193
	v_cvt_pk_bf16_f32 v191, v194, v195
	v_cvt_pk_bf16_f32 v192, v196, v197
	v_cvt_pk_bf16_f32 v193, v198, v199
	s_nop 1
	v_mfma_f32_32x32x16_bf16 v[50:65], v[170:173], v[186:189], v[50:65]
	v_mfma_f32_32x32x16_bf16 v[34:49], v[174:177], v[186:189], v[34:49]
	v_mfma_f32_32x32x16_bf16 v[18:33], v[178:181], v[186:189], v[18:33]
	v_mfma_f32_32x32x16_bf16 v[2:17], v[182:185], v[186:189], v[2:17]
	v_mfma_f32_32x32x16_bf16 v[114:129], v[170:173], v[190:193], v[114:129]
	v_mfma_f32_32x32x16_bf16 v[98:113], v[174:177], v[190:193], v[98:113]
	v_mfma_f32_32x32x16_bf16 v[82:97], v[178:181], v[190:193], v[82:97]
	v_mfma_f32_32x32x16_bf16 v[66:81], v[182:185], v[190:193], v[66:81]
	v_add_u32_e32 v196, v200, v163
	v_add_u32_e32 v201, v159, v162
	ds_read_b64 v[186:187], v196
	ds_read_b128 v[170:173], v201 offset:49152
	ds_read_b128 v[174:177], v201 offset:51200
	ds_read_b128 v[178:181], v201 offset:53248
	ds_read_b128 v[182:185], v201 offset:55296
	s_waitcnt lgkmcnt(0)
	v_cvt_pk_f32_fp8_e32 v[188:189], v186
	v_cvt_pk_f32_fp8_sdwa v[190:191], v186 src0_sel:WORD_1
	v_cvt_pk_f32_fp8_e32 v[192:193], v187
	v_cvt_pk_f32_fp8_sdwa v[194:195], v187 src0_sel:WORD_1
	v_cvt_pk_bf16_f32 v186, v188, v189
	v_cvt_pk_bf16_f32 v187, v190, v191
	v_cvt_pk_bf16_f32 v188, v192, v193
	v_cvt_pk_bf16_f32 v189, v194, v195
	ds_read_b64 v[190:191], v196 offset:8192
	v_mfma_f32_32x32x16_bf16 v[50:65], v[170:173], v[186:189], v[50:65]
	s_waitcnt lgkmcnt(0)
	v_cvt_pk_f32_fp8_e32 v[192:193], v190
	v_cvt_pk_f32_fp8_e32 v[194:195], v191
	v_mfma_f32_32x32x16_bf16 v[34:49], v[174:177], v[186:189], v[34:49]
	v_mfma_f32_32x32x16_bf16 v[18:33], v[178:181], v[186:189], v[18:33]
	v_mfma_f32_32x32x16_bf16 v[2:17], v[182:185], v[186:189], v[2:17]
	v_cvt_pk_f32_fp8_sdwa v[188:189], v190 src0_sel:WORD_1
	v_cvt_pk_f32_fp8_sdwa v[190:191], v191 src0_sel:WORD_1
	v_cvt_pk_bf16_f32 v186, v192, v193
	v_cvt_pk_bf16_f32 v187, v188, v189
	v_cvt_pk_bf16_f32 v188, v194, v195
	v_cvt_pk_bf16_f32 v189, v190, v191
	s_nop 0
	v_mfma_f32_32x32x16_bf16 v[114:129], v[170:173], v[186:189], v[114:129]
	v_mfma_f32_32x32x16_bf16 v[98:113], v[174:177], v[186:189], v[98:113]
	v_mfma_f32_32x32x16_bf16 v[82:97], v[178:181], v[186:189], v[82:97]
	v_mfma_f32_32x32x16_bf16 v[66:81], v[182:185], v[186:189], v[66:81]
	s_add_u32 s52, s12, s10
	s_waitcnt vmcnt(6)
	s_addc_u32 s53, s13, 0
	s_mov_b32 m0, s50
	s_waitcnt lgkmcnt(0)
	s_barrier
	v_lshl_add_u64 v[170:171], s[52:53], 0, v[146:147]
	global_load_lds_dwordx4 v[170:171], off
	v_lshl_add_u64 v[170:171], s[52:53], 0, v[156:157]
	s_add_i32 m0, s50, 0x2000
	s_addk_i32 s49, 0x402
	global_load_lds_dwordx4 v[170:171], off
	s_bfe_u32 s10, s49, 0x70009
	s_mul_i32 s10, s10, 3
	s_sub_i32 s10, s36, s10
	s_add_i32 s10, s10, 6
	s_and_b32 s10, s10, 0xff
	s_lshl_b32 s10, s10, 14
	s_add_i32 s36, s39, s10
	s_waitcnt vmcnt(6)
	s_cmp_lt_u32 s37, 12
	v_cvt_pk_bf16_f32 v138, v138, v142
	ds_write_b32 v167, v138 offset:49152
	v_cvt_pk_bf16_f32 v138, v139, v143
	s_cselect_b32 s10, s35, 0x1e0
	ds_write_b32 v167, v138 offset:49216
	v_cvt_pk_bf16_f32 v138, v140, v144
	s_lshl_b64 s[50:51], s[10:11], 13
	ds_write_b32 v167, v138 offset:49280
	v_cvt_pk_bf16_f32 v138, v141, v145
	ds_write_b32 v167, v138 offset:49344
	v_lshl_add_u64 v[142:143], v[154:155], 0, s[50:51]
	global_load_dwordx4 v[138:141], v[142:143], off sc1 nt
	v_lshl_add_u64 v[142:143], v[142:143], 0, s[20:21]
	global_load_dwordx4 v[142:145], v[142:143], off sc1 nt
	v_add_u32_e32 v200, s36, v158
	v_add_u32_e32 v196, v200, v161
	ds_read_b64 v[186:187], v196
	ds_read_b128 v[170:173], v169 offset:57344
	ds_read_b128 v[174:177], v169 offset:59392
	ds_read_b128 v[178:181], v169 offset:61440
	ds_read_b128 v[182:185], v169 offset:63488
	s_waitcnt lgkmcnt(0)
	v_cvt_pk_f32_fp8_e32 v[188:189], v186
	v_cvt_pk_f32_fp8_sdwa v[190:191], v186 src0_sel:WORD_1
	v_cvt_pk_f32_fp8_e32 v[192:193], v187
	v_cvt_pk_f32_fp8_sdwa v[194:195], v187 src0_sel:WORD_1
	v_cvt_pk_bf16_f32 v186, v188, v189
	v_cvt_pk_bf16_f32 v187, v190, v191
	v_cvt_pk_bf16_f32 v188, v192, v193
	v_cvt_pk_bf16_f32 v189, v194, v195
	ds_read_b64 v[190:191], v196 offset:8192
	s_waitcnt lgkmcnt(0)
	v_cvt_pk_f32_fp8_e32 v[192:193], v190
	v_cvt_pk_f32_fp8_sdwa v[194:195], v190 src0_sel:WORD_1
	v_cvt_pk_f32_fp8_e32 v[196:197], v191
	v_cvt_pk_f32_fp8_sdwa v[198:199], v191 src0_sel:WORD_1
	v_cvt_pk_bf16_f32 v190, v192, v193
	v_cvt_pk_bf16_f32 v191, v194, v195
	v_cvt_pk_bf16_f32 v192, v196, v197
	v_cvt_pk_bf16_f32 v193, v198, v199
	s_nop 1
	v_mfma_f32_32x32x16_bf16 v[50:65], v[170:173], v[186:189], v[50:65]
	v_mfma_f32_32x32x16_bf16 v[34:49], v[174:177], v[186:189], v[34:49]
	v_mfma_f32_32x32x16_bf16 v[18:33], v[178:181], v[186:189], v[18:33]
	v_mfma_f32_32x32x16_bf16 v[2:17], v[182:185], v[186:189], v[2:17]
	v_mfma_f32_32x32x16_bf16 v[114:129], v[170:173], v[190:193], v[114:129]
	v_mfma_f32_32x32x16_bf16 v[98:113], v[174:177], v[190:193], v[98:113]
	v_mfma_f32_32x32x16_bf16 v[82:97], v[178:181], v[190:193], v[82:97]
	v_mfma_f32_32x32x16_bf16 v[66:81], v[182:185], v[190:193], v[66:81]
	v_add_u32_e32 v169, v200, v163
	ds_read_b64 v[186:187], v169
	ds_read_b128 v[170:173], v201 offset:57344
	ds_read_b128 v[174:177], v201 offset:59392
	ds_read_b128 v[178:181], v201 offset:61440
	ds_read_b128 v[182:185], v201 offset:63488
	s_waitcnt lgkmcnt(0)
	v_cvt_pk_f32_fp8_e32 v[188:189], v186
	v_cvt_pk_f32_fp8_sdwa v[190:191], v186 src0_sel:WORD_1
	v_cvt_pk_f32_fp8_e32 v[192:193], v187
	v_cvt_pk_f32_fp8_sdwa v[194:195], v187 src0_sel:WORD_1
	v_cvt_pk_bf16_f32 v186, v188, v189
	v_cvt_pk_bf16_f32 v187, v190, v191
	v_cvt_pk_bf16_f32 v188, v192, v193
	v_cvt_pk_bf16_f32 v189, v194, v195
	ds_read_b64 v[190:191], v169 offset:8192
	v_mfma_f32_32x32x16_bf16 v[50:65], v[170:173], v[186:189], v[50:65]
	s_waitcnt lgkmcnt(0)
	v_cvt_pk_f32_fp8_e32 v[192:193], v190
	v_cvt_pk_f32_fp8_e32 v[194:195], v191
	v_mfma_f32_32x32x16_bf16 v[34:49], v[174:177], v[186:189], v[34:49]
	v_mfma_f32_32x32x16_bf16 v[18:33], v[178:181], v[186:189], v[18:33]
	v_mfma_f32_32x32x16_bf16 v[2:17], v[182:185], v[186:189], v[2:17]
	v_cvt_pk_f32_fp8_sdwa v[188:189], v190 src0_sel:WORD_1
	v_cvt_pk_f32_fp8_sdwa v[190:191], v191 src0_sel:WORD_1
	v_cvt_pk_bf16_f32 v186, v192, v193
	v_cvt_pk_bf16_f32 v187, v188, v189
	v_cvt_pk_bf16_f32 v188, v194, v195
	v_cvt_pk_bf16_f32 v189, v190, v191
	s_nop 0
	v_mfma_f32_32x32x16_bf16 v[114:129], v[170:173], v[186:189], v[114:129]
	v_mfma_f32_32x32x16_bf16 v[98:113], v[174:177], v[186:189], v[98:113]
	v_mfma_f32_32x32x16_bf16 v[82:97], v[178:181], v[186:189], v[82:97]
	v_mfma_f32_32x32x16_bf16 v[66:81], v[182:185], v[186:189], v[66:81]
	s_add_u32 s50, s12, s10
	s_waitcnt vmcnt(6)
	s_addc_u32 s51, s13, 0
	s_mov_b32 m0, s36
	s_waitcnt lgkmcnt(0)
	s_barrier
	v_lshl_add_u64 v[170:171], s[50:51], 0, v[146:147]
	global_load_lds_dwordx4 v[170:171], off
	v_lshl_add_u64 v[170:171], s[50:51], 0, v[156:157]
	s_add_i32 m0, s36, 0x2000
	s_add_i32 s35, s35, 64
	global_load_lds_dwordx4 v[170:171], off
	s_cmp_gt_u32 s37, 13
	s_mov_b32 s36, s37
	s_cbranch_scc0 .LBB0_1091
	s_branch .Lmoe_X_1091

.Lmoe_G2_1091:
	s_mul_i32 s49, s36, 0xab
	s_add_i32 s10, s49, 0x357
	s_bfe_u32 s10, s10, 0x70009
	s_mul_i32 s10, s10, 3
	s_sub_i32 s10, s36, s10
	s_add_i32 s10, s10, 5
	s_and_b32 s10, s10, 0xff
	s_lshl_b32 s10, s10, 14
	s_add_i32 s50, s39, s10
	s_add_i32 s37, s36, 2
	v_add_u32_e32 v200, s50, v158
	v_add_u32_e32 v196, v200, v161
	v_add_u32_e32 v169, v159, v160
	ds_read_b64 v[186:187], v196
	ds_read_b128 v[170:173], v169 offset:49152
	ds_read_b128 v[174:177], v169 offset:51200
	ds_read_b128 v[178:181], v169 offset:53248
	ds_read_b128 v[182:185], v169 offset:55296
	s_waitcnt lgkmcnt(0)
	v_cvt_pk_f32_fp8_e32 v[188:189], v186
	v_cvt_pk_f32_fp8_sdwa v[190:191], v186 src0_sel:WORD_1
	v_cvt_pk_f32_fp8_e32 v[192:193], v187
	v_cvt_pk_f32_fp8_sdwa v[194:195], v187 src0_sel:WORD_1
	v_cvt_pk_bf16_f32 v186, v188, v189
	v_cvt_pk_bf16_f32 v187, v190, v191
	v_cvt_pk_bf16_f32 v188, v192, v193
	v_cvt_pk_bf16_f32 v189, v194, v195
	ds_read_b64 v[190:191], v196 offset:8192
	s_waitcnt lgkmcnt(0)
	v_cvt_pk_f32_fp8_e32 v[192:193], v190
	v_cvt_pk_f32_fp8_sdwa v[194:195], v190 src0_sel:WORD_1
	v_cvt_pk_f32_fp8_e32 v[196:197], v191
	v_cvt_pk_f32_fp8_sdwa v[198:199], v191 src0_sel:WORD_1
	v_cvt_pk_bf16_f32 v190, v192, v193
	v_cvt_pk_bf16_f32 v191, v194, v195
	v_cvt_pk_bf16_f32 v192, v196, v197
	v_cvt_pk_bf16_f32 v193, v198, v199
	s_nop 1
	v_mfma_f32_32x32x16_bf16 v[50:65], v[170:173], v[186:189], v[50:65]
	v_mfma_f32_32x32x16_bf16 v[34:49], v[174:177], v[186:189], v[34:49]
	v_mfma_f32_32x32x16_bf16 v[18:33], v[178:181], v[186:189], v[18:33]
	v_mfma_f32_32x32x16_bf16 v[2:17], v[182:185], v[186:189], v[2:17]
	v_mfma_f32_32x32x16_bf16 v[114:129], v[170:173], v[190:193], v[114:129]
	v_mfma_f32_32x32x16_bf16 v[98:113], v[174:177], v[190:193], v[98:113]
	v_mfma_f32_32x32x16_bf16 v[82:97], v[178:181], v[190:193], v[82:97]
	v_mfma_f32_32x32x16_bf16 v[66:81], v[182:185], v[190:193], v[66:81]
	s_waitcnt vmcnt(6)
	s_sub_i32 s10, s35, 32
	v_cvt_pk_bf16_f32 v130, v130, v134
	s_cmp_lt_u32 s37, 13
	ds_write_b32 v167, v130 offset:57344
	v_cvt_pk_bf16_f32 v130, v131, v135
	s_cselect_b32 s10, s10, 0x1e0
	ds_write_b32 v167, v130 offset:57408
	v_cvt_pk_bf16_f32 v130, v132, v136
	s_lshl_b64 s[52:53], s[10:11], 13
	ds_write_b32 v167, v130 offset:57472
	v_cvt_pk_bf16_f32 v130, v133, v137
	ds_write_b32 v167, v130 offset:57536
	v_lshl_add_u64 v[134:135], v[154:155], 0, s[52:53]
	global_load_dwordx4 v[130:133], v[134:135], off sc1 nt
	v_lshl_add_u64 v[134:135], v[134:135], 0, s[20:21]
	global_load_dwordx4 v[134:137], v[134:135], off sc1 nt
	v_add_u32_e32 v196, v200, v163
	v_add_u32_e32 v201, v159, v162
	ds_read_b64 v[186:187], v196
	ds_read_b128 v[170:173], v201 offset:49152
	ds_read_b128 v[174:177], v201 offset:51200
	ds_read_b128 v[178:181], v201 offset:53248
	ds_read_b128 v[182:185], v201 offset:55296
	s_waitcnt lgkmcnt(0)
	v_cvt_pk_f32_fp8_e32 v[188:189], v186
	v_cvt_pk_f32_fp8_sdwa v[190:191], v186 src0_sel:WORD_1
	v_cvt_pk_f32_fp8_e32 v[192:193], v187
	v_cvt_pk_f32_fp8_sdwa v[194:195], v187 src0_sel:WORD_1
	v_cvt_pk_bf16_f32 v186, v188, v189
	v_cvt_pk_bf16_f32 v187, v190, v191
	v_cvt_pk_bf16_f32 v188, v192, v193
	v_cvt_pk_bf16_f32 v189, v194, v195
	ds_read_b64 v[190:191], v196 offset:8192
	v_mfma_f32_32x32x16_bf16 v[50:65], v[170:173], v[186:189], v[50:65]
	s_waitcnt lgkmcnt(0)
	v_cvt_pk_f32_fp8_e32 v[192:193], v190
	v_cvt_pk_f32_fp8_e32 v[194:195], v191
	v_mfma_f32_32x32x16_bf16 v[34:49], v[174:177], v[186:189], v[34:49]
	v_mfma_f32_32x32x16_bf16 v[18:33], v[178:181], v[186:189], v[18:33]
	v_mfma_f32_32x32x16_bf16 v[2:17], v[182:185], v[186:189], v[2:17]
	v_cvt_pk_f32_fp8_sdwa v[188:189], v190 src0_sel:WORD_1
	v_cvt_pk_f32_fp8_sdwa v[190:191], v191 src0_sel:WORD_1
	v_cvt_pk_bf16_f32 v186, v192, v193
	v_cvt_pk_bf16_f32 v187, v188, v189
	v_cvt_pk_bf16_f32 v188, v194, v195
	v_cvt_pk_bf16_f32 v189, v190, v191
	s_nop 0
	v_mfma_f32_32x32x16_bf16 v[114:129], v[170:173], v[186:189], v[114:129]
	v_mfma_f32_32x32x16_bf16 v[98:113], v[174:177], v[186:189], v[98:113]
	v_mfma_f32_32x32x16_bf16 v[82:97], v[178:181], v[186:189], v[82:97]
	v_mfma_f32_32x32x16_bf16 v[66:81], v[182:185], v[186:189], v[66:81]
	s_add_u32 s52, s12, s10
	s_waitcnt vmcnt(6)
	s_addc_u32 s53, s13, 0
	s_mov_b32 m0, s50
	s_waitcnt lgkmcnt(0)
	s_barrier
	v_lshl_add_u64 v[170:171], s[52:53], 0, v[146:147]
	global_load_lds_dwordx4 v[170:171], off
	v_lshl_add_u64 v[170:171], s[52:53], 0, v[156:157]
	s_add_i32 m0, s50, 0x2000
	s_addk_i32 s49, 0x402
	global_load_lds_dwordx4 v[170:171], off
	s_bfe_u32 s10, s49, 0x70009
	s_mul_i32 s10, s10, 3
	s_sub_i32 s10, s36, s10
	s_add_i32 s10, s10, 6
	s_and_b32 s10, s10, 0xff
	s_lshl_b32 s10, s10, 14
	s_add_i32 s36, s39, s10
	v_add_u32_e32 v200, s36, v158
	v_add_u32_e32 v196, v200, v161
	ds_read_b64 v[186:187], v196
	ds_read_b128 v[170:173], v169 offset:57344
	ds_read_b128 v[174:177], v169 offset:59392
	ds_read_b128 v[178:181], v169 offset:61440
	ds_read_b128 v[182:185], v169 offset:63488
	s_waitcnt lgkmcnt(0)
	v_cvt_pk_f32_fp8_e32 v[188:189], v186
	v_cvt_pk_f32_fp8_sdwa v[190:191], v186 src0_sel:WORD_1
	v_cvt_pk_f32_fp8_e32 v[192:193], v187
	v_cvt_pk_f32_fp8_sdwa v[194:195], v187 src0_sel:WORD_1
	v_cvt_pk_bf16_f32 v186, v188, v189
	v_cvt_pk_bf16_f32 v187, v190, v191
	v_cvt_pk_bf16_f32 v188, v192, v193
	v_cvt_pk_bf16_f32 v189, v194, v195
	ds_read_b64 v[190:191], v196 offset:8192
	s_waitcnt lgkmcnt(0)
	v_cvt_pk_f32_fp8_e32 v[192:193], v190
	v_cvt_pk_f32_fp8_sdwa v[194:195], v190 src0_sel:WORD_1
	v_cvt_pk_f32_fp8_e32 v[196:197], v191
	v_cvt_pk_f32_fp8_sdwa v[198:199], v191 src0_sel:WORD_1
	v_cvt_pk_bf16_f32 v190, v192, v193
	v_cvt_pk_bf16_f32 v191, v194, v195
	v_cvt_pk_bf16_f32 v192, v196, v197
	v_cvt_pk_bf16_f32 v193, v198, v199
	s_nop 1
	v_mfma_f32_32x32x16_bf16 v[50:65], v[170:173], v[186:189], v[50:65]
	v_mfma_f32_32x32x16_bf16 v[34:49], v[174:177], v[186:189], v[34:49]
	v_mfma_f32_32x32x16_bf16 v[18:33], v[178:181], v[186:189], v[18:33]
	v_mfma_f32_32x32x16_bf16 v[2:17], v[182:185], v[186:189], v[2:17]
	v_mfma_f32_32x32x16_bf16 v[114:129], v[170:173], v[190:193], v[114:129]
	v_mfma_f32_32x32x16_bf16 v[98:113], v[174:177], v[190:193], v[98:113]
	v_mfma_f32_32x32x16_bf16 v[82:97], v[178:181], v[190:193], v[82:97]
	v_mfma_f32_32x32x16_bf16 v[66:81], v[182:185], v[190:193], v[66:81]
	s_waitcnt vmcnt(6)
	s_cmp_lt_u32 s37, 12
	v_cvt_pk_bf16_f32 v138, v138, v142
	ds_write_b32 v167, v138 offset:49152
	v_cvt_pk_bf16_f32 v138, v139, v143
	s_cselect_b32 s10, s35, 0x1e0
	ds_write_b32 v167, v138 offset:49216
	v_cvt_pk_bf16_f32 v138, v140, v144
	s_lshl_b64 s[50:51], s[10:11], 13
	ds_write_b32 v167, v138 offset:49280
	v_cvt_pk_bf16_f32 v138, v141, v145
	ds_write_b32 v167, v138 offset:49344
	v_lshl_add_u64 v[142:143], v[154:155], 0, s[50:51]
	global_load_dwordx4 v[138:141], v[142:143], off sc1 nt
	v_lshl_add_u64 v[142:143], v[142:143], 0, s[20:21]
	global_load_dwordx4 v[142:145], v[142:143], off sc1 nt
	v_add_u32_e32 v169, v200, v163
	ds_read_b64 v[186:187], v169
	ds_read_b128 v[170:173], v201 offset:57344
	ds_read_b128 v[174:177], v201 offset:59392
	ds_read_b128 v[178:181], v201 offset:61440
	ds_read_b128 v[182:185], v201 offset:63488
	s_waitcnt lgkmcnt(0)
	v_cvt_pk_f32_fp8_e32 v[188:189], v186
	v_cvt_pk_f32_fp8_sdwa v[190:191], v186 src0_sel:WORD_1
	v_cvt_pk_f32_fp8_e32 v[192:193], v187
	v_cvt_pk_f32_fp8_sdwa v[194:195], v187 src0_sel:WORD_1
	v_cvt_pk_bf16_f32 v186, v188, v189
	v_cvt_pk_bf16_f32 v187, v190, v191
	v_cvt_pk_bf16_f32 v188, v192, v193
	v_cvt_pk_bf16_f32 v189, v194, v195
	ds_read_b64 v[190:191], v169 offset:8192
	v_mfma_f32_32x32x16_bf16 v[50:65], v[170:173], v[186:189], v[50:65]
	s_waitcnt lgkmcnt(0)
	v_cvt_pk_f32_fp8_e32 v[192:193], v190
	v_cvt_pk_f32_fp8_e32 v[194:195], v191
	v_mfma_f32_32x32x16_bf16 v[34:49], v[174:177], v[186:189], v[34:49]
	v_mfma_f32_32x32x16_bf16 v[18:33], v[178:181], v[186:189], v[18:33]
	v_mfma_f32_32x32x16_bf16 v[2:17], v[182:185], v[186:189], v[2:17]
	v_cvt_pk_f32_fp8_sdwa v[188:189], v190 src0_sel:WORD_1
	v_cvt_pk_f32_fp8_sdwa v[190:191], v191 src0_sel:WORD_1
	v_cvt_pk_bf16_f32 v186, v192, v193
	v_cvt_pk_bf16_f32 v187, v188, v189
	v_cvt_pk_bf16_f32 v188, v194, v195
	v_cvt_pk_bf16_f32 v189, v190, v191
	s_nop 0
	v_mfma_f32_32x32x16_bf16 v[114:129], v[170:173], v[186:189], v[114:129]
	v_mfma_f32_32x32x16_bf16 v[98:113], v[174:177], v[186:189], v[98:113]
	v_mfma_f32_32x32x16_bf16 v[82:97], v[178:181], v[186:189], v[82:97]
	v_mfma_f32_32x32x16_bf16 v[66:81], v[182:185], v[186:189], v[66:81]
	s_add_u32 s50, s12, s10
	s_waitcnt vmcnt(6)
	s_addc_u32 s51, s13, 0
	s_mov_b32 m0, s36
	s_waitcnt lgkmcnt(0)
	s_barrier
	v_lshl_add_u64 v[170:171], s[50:51], 0, v[146:147]
	global_load_lds_dwordx4 v[170:171], off
	v_lshl_add_u64 v[170:171], s[50:51], 0, v[156:157]
	s_add_i32 m0, s36, 0x2000
	s_add_i32 s35, s35, 64
	global_load_lds_dwordx4 v[170:171], off
	s_cmp_gt_u32 s37, 13
	s_mov_b32 s36, s37
	s_cbranch_scc0 .Lmoe_G2_1091
	s_branch .Lmoe_X_1091
.Lmoe_G3_1091:
	s_mul_i32 s49, s36, 0xab
	s_add_i32 s10, s49, 0x357
	s_bfe_u32 s10, s10, 0x70009
	s_mul_i32 s10, s10, 3
	s_sub_i32 s10, s36, s10
	s_add_i32 s10, s10, 5
	s_and_b32 s10, s10, 0xff
	s_lshl_b32 s10, s10, 14
	s_add_i32 s50, s39, s10
	s_add_i32 s37, s36, 2
	v_add_u32_e32 v200, s50, v158
	v_add_u32_e32 v196, v200, v161
	v_add_u32_e32 v169, v159, v160
	ds_read_b64 v[186:187], v196
	ds_read_b128 v[170:173], v169 offset:49152
	ds_read_b128 v[174:177], v169 offset:51200
	ds_read_b128 v[178:181], v169 offset:53248
	ds_read_b128 v[182:185], v169 offset:55296
	s_waitcnt lgkmcnt(0)
	v_cvt_pk_f32_fp8_e32 v[188:189], v186
	v_cvt_pk_f32_fp8_sdwa v[190:191], v186 src0_sel:WORD_1
	v_cvt_pk_f32_fp8_e32 v[192:193], v187
	v_cvt_pk_f32_fp8_sdwa v[194:195], v187 src0_sel:WORD_1
	v_cvt_pk_bf16_f32 v186, v188, v189
	v_cvt_pk_bf16_f32 v187, v190, v191
	v_cvt_pk_bf16_f32 v188, v192, v193
	v_cvt_pk_bf16_f32 v189, v194, v195
	ds_read_b64 v[190:191], v196 offset:8192
	s_waitcnt lgkmcnt(0)
	v_cvt_pk_f32_fp8_e32 v[192:193], v190
	v_cvt_pk_f32_fp8_sdwa v[194:195], v190 src0_sel:WORD_1
	v_cvt_pk_f32_fp8_e32 v[196:197], v191
	v_cvt_pk_f32_fp8_sdwa v[198:199], v191 src0_sel:WORD_1
	v_cvt_pk_bf16_f32 v190, v192, v193
	v_cvt_pk_bf16_f32 v191, v194, v195
	v_cvt_pk_bf16_f32 v192, v196, v197
	v_cvt_pk_bf16_f32 v193, v198, v199
	s_nop 1
	v_mfma_f32_32x32x16_bf16 v[50:65], v[170:173], v[186:189], v[50:65]
	v_mfma_f32_32x32x16_bf16 v[34:49], v[174:177], v[186:189], v[34:49]
	v_mfma_f32_32x32x16_bf16 v[18:33], v[178:181], v[186:189], v[18:33]
	v_mfma_f32_32x32x16_bf16 v[2:17], v[182:185], v[186:189], v[2:17]
	v_mfma_f32_32x32x16_bf16 v[114:129], v[170:173], v[190:193], v[114:129]
	v_mfma_f32_32x32x16_bf16 v[98:113], v[174:177], v[190:193], v[98:113]
	v_mfma_f32_32x32x16_bf16 v[82:97], v[178:181], v[190:193], v[82:97]
	v_mfma_f32_32x32x16_bf16 v[66:81], v[182:185], v[190:193], v[66:81]
	v_add_u32_e32 v196, v200, v163
	v_add_u32_e32 v201, v159, v162
	ds_read_b64 v[186:187], v196
	ds_read_b128 v[170:173], v201 offset:49152
	ds_read_b128 v[174:177], v201 offset:51200
	ds_read_b128 v[178:181], v201 offset:53248
	ds_read_b128 v[182:185], v201 offset:55296
	s_waitcnt lgkmcnt(0)
	v_cvt_pk_f32_fp8_e32 v[188:189], v186
	v_cvt_pk_f32_fp8_sdwa v[190:191], v186 src0_sel:WORD_1
	v_cvt_pk_f32_fp8_e32 v[192:193], v187
	v_cvt_pk_f32_fp8_sdwa v[194:195], v187 src0_sel:WORD_1
	v_cvt_pk_bf16_f32 v186, v188, v189
	v_cvt_pk_bf16_f32 v187, v190, v191
	v_cvt_pk_bf16_f32 v188, v192, v193
	v_cvt_pk_bf16_f32 v189, v194, v195
	ds_read_b64 v[190:191], v196 offset:8192
	v_mfma_f32_32x32x16_bf16 v[50:65], v[170:173], v[186:189], v[50:65]
	s_waitcnt lgkmcnt(0)
	v_cvt_pk_f32_fp8_e32 v[192:193], v190
	v_cvt_pk_f32_fp8_e32 v[194:195], v191
	v_mfma_f32_32x32x16_bf16 v[34:49], v[174:177], v[186:189], v[34:49]
	v_mfma_f32_32x32x16_bf16 v[18:33], v[178:181], v[186:189], v[18:33]
	v_mfma_f32_32x32x16_bf16 v[2:17], v[182:185], v[186:189], v[2:17]
	v_cvt_pk_f32_fp8_sdwa v[188:189], v190 src0_sel:WORD_1
	v_cvt_pk_f32_fp8_sdwa v[190:191], v191 src0_sel:WORD_1
	v_cvt_pk_bf16_f32 v186, v192, v193
	v_cvt_pk_bf16_f32 v187, v188, v189
	v_cvt_pk_bf16_f32 v188, v194, v195
	v_cvt_pk_bf16_f32 v189, v190, v191
	s_nop 0
	v_mfma_f32_32x32x16_bf16 v[114:129], v[170:173], v[186:189], v[114:129]
	v_mfma_f32_32x32x16_bf16 v[98:113], v[174:177], v[186:189], v[98:113]
	v_mfma_f32_32x32x16_bf16 v[82:97], v[178:181], v[186:189], v[82:97]
	v_mfma_f32_32x32x16_bf16 v[66:81], v[182:185], v[186:189], v[66:81]
	s_waitcnt vmcnt(6)
	s_sub_i32 s10, s35, 32
	v_cvt_pk_bf16_f32 v130, v130, v134
	s_cmp_lt_u32 s37, 13
	ds_write_b32 v167, v130 offset:57344
	v_cvt_pk_bf16_f32 v130, v131, v135
	s_cselect_b32 s10, s10, 0x1e0
	ds_write_b32 v167, v130 offset:57408
	v_cvt_pk_bf16_f32 v130, v132, v136
	s_lshl_b64 s[52:53], s[10:11], 13
	ds_write_b32 v167, v130 offset:57472
	v_cvt_pk_bf16_f32 v130, v133, v137
	ds_write_b32 v167, v130 offset:57536
	v_lshl_add_u64 v[134:135], v[154:155], 0, s[52:53]
	global_load_dwordx4 v[130:133], v[134:135], off sc1 nt
	v_lshl_add_u64 v[134:135], v[134:135], 0, s[20:21]
	global_load_dwordx4 v[134:137], v[134:135], off sc1 nt
	s_add_u32 s52, s12, s10
	s_waitcnt vmcnt(6)
	s_addc_u32 s53, s13, 0
	s_mov_b32 m0, s50
	s_waitcnt lgkmcnt(0)
	s_barrier
	v_lshl_add_u64 v[170:171], s[52:53], 0, v[146:147]
	global_load_lds_dwordx4 v[170:171], off
	v_lshl_add_u64 v[170:171], s[52:53], 0, v[156:157]
	s_add_i32 m0, s50, 0x2000
	s_addk_i32 s49, 0x402
	global_load_lds_dwordx4 v[170:171], off
	s_bfe_u32 s10, s49, 0x70009
	s_mul_i32 s10, s10, 3
	s_sub_i32 s10, s36, s10
	s_add_i32 s10, s10, 6
	s_and_b32 s10, s10, 0xff
	s_lshl_b32 s10, s10, 14
	s_add_i32 s36, s39, s10
	v_add_u32_e32 v200, s36, v158
	v_add_u32_e32 v196, v200, v161
	ds_read_b64 v[186:187], v196
	ds_read_b128 v[170:173], v169 offset:57344
	ds_read_b128 v[174:177], v169 offset:59392
	ds_read_b128 v[178:181], v169 offset:61440
	ds_read_b128 v[182:185], v169 offset:63488
	s_waitcnt lgkmcnt(0)
	v_cvt_pk_f32_fp8_e32 v[188:189], v186
	v_cvt_pk_f32_fp8_sdwa v[190:191], v186 src0_sel:WORD_1
	v_cvt_pk_f32_fp8_e32 v[192:193], v187
	v_cvt_pk_f32_fp8_sdwa v[194:195], v187 src0_sel:WORD_1
	v_cvt_pk_bf16_f32 v186, v188, v189
	v_cvt_pk_bf16_f32 v187, v190, v191
	v_cvt_pk_bf16_f32 v188, v192, v193
	v_cvt_pk_bf16_f32 v189, v194, v195
	ds_read_b64 v[190:191], v196 offset:8192
	s_waitcnt lgkmcnt(0)
	v_cvt_pk_f32_fp8_e32 v[192:193], v190
	v_cvt_pk_f32_fp8_sdwa v[194:195], v190 src0_sel:WORD_1
	v_cvt_pk_f32_fp8_e32 v[196:197], v191
	v_cvt_pk_f32_fp8_sdwa v[198:199], v191 src0_sel:WORD_1
	v_cvt_pk_bf16_f32 v190, v192, v193
	v_cvt_pk_bf16_f32 v191, v194, v195
	v_cvt_pk_bf16_f32 v192, v196, v197
	v_cvt_pk_bf16_f32 v193, v198, v199
	s_nop 1
	v_mfma_f32_32x32x16_bf16 v[50:65], v[170:173], v[186:189], v[50:65]
	v_mfma_f32_32x32x16_bf16 v[34:49], v[174:177], v[186:189], v[34:49]
	v_mfma_f32_32x32x16_bf16 v[18:33], v[178:181], v[186:189], v[18:33]
	v_mfma_f32_32x32x16_bf16 v[2:17], v[182:185], v[186:189], v[2:17]
	v_mfma_f32_32x32x16_bf16 v[114:129], v[170:173], v[190:193], v[114:129]
	v_mfma_f32_32x32x16_bf16 v[98:113], v[174:177], v[190:193], v[98:113]
	v_mfma_f32_32x32x16_bf16 v[82:97], v[178:181], v[190:193], v[82:97]
	v_mfma_f32_32x32x16_bf16 v[66:81], v[182:185], v[190:193], v[66:81]
	v_add_u32_e32 v169, v200, v163
	ds_read_b64 v[186:187], v169
	ds_read_b128 v[170:173], v201 offset:57344
	ds_read_b128 v[174:177], v201 offset:59392
	ds_read_b128 v[178:181], v201 offset:61440
	ds_read_b128 v[182:185], v201 offset:63488
	s_waitcnt lgkmcnt(0)
	v_cvt_pk_f32_fp8_e32 v[188:189], v186
	v_cvt_pk_f32_fp8_sdwa v[190:191], v186 src0_sel:WORD_1
	v_cvt_pk_f32_fp8_e32 v[192:193], v187
	v_cvt_pk_f32_fp8_sdwa v[194:195], v187 src0_sel:WORD_1
	v_cvt_pk_bf16_f32 v186, v188, v189
	v_cvt_pk_bf16_f32 v187, v190, v191
	v_cvt_pk_bf16_f32 v188, v192, v193
	v_cvt_pk_bf16_f32 v189, v194, v195
	ds_read_b64 v[190:191], v169 offset:8192
	v_mfma_f32_32x32x16_bf16 v[50:65], v[170:173], v[186:189], v[50:65]
	s_waitcnt lgkmcnt(0)
	v_cvt_pk_f32_fp8_e32 v[192:193], v190
	v_cvt_pk_f32_fp8_e32 v[194:195], v191
	v_mfma_f32_32x32x16_bf16 v[34:49], v[174:177], v[186:189], v[34:49]
	v_mfma_f32_32x32x16_bf16 v[18:33], v[178:181], v[186:189], v[18:33]
	v_mfma_f32_32x32x16_bf16 v[2:17], v[182:185], v[186:189], v[2:17]
	v_cvt_pk_f32_fp8_sdwa v[188:189], v190 src0_sel:WORD_1
	v_cvt_pk_f32_fp8_sdwa v[190:191], v191 src0_sel:WORD_1
	v_cvt_pk_bf16_f32 v186, v192, v193
	v_cvt_pk_bf16_f32 v187, v188, v189
	v_cvt_pk_bf16_f32 v188, v194, v195
	v_cvt_pk_bf16_f32 v189, v190, v191
	s_nop 0
	v_mfma_f32_32x32x16_bf16 v[114:129], v[170:173], v[186:189], v[114:129]
	v_mfma_f32_32x32x16_bf16 v[98:113], v[174:177], v[186:189], v[98:113]
	v_mfma_f32_32x32x16_bf16 v[82:97], v[178:181], v[186:189], v[82:97]
	v_mfma_f32_32x32x16_bf16 v[66:81], v[182:185], v[186:189], v[66:81]
	s_waitcnt vmcnt(6)
	s_cmp_lt_u32 s37, 12
	v_cvt_pk_bf16_f32 v138, v138, v142
	ds_write_b32 v167, v138 offset:49152
	v_cvt_pk_bf16_f32 v138, v139, v143
	s_cselect_b32 s10, s35, 0x1e0
	ds_write_b32 v167, v138 offset:49216
	v_cvt_pk_bf16_f32 v138, v140, v144
	s_lshl_b64 s[50:51], s[10:11], 13
	ds_write_b32 v167, v138 offset:49280
	v_cvt_pk_bf16_f32 v138, v141, v145
	ds_write_b32 v167, v138 offset:49344
	v_lshl_add_u64 v[142:143], v[154:155], 0, s[50:51]
	global_load_dwordx4 v[138:141], v[142:143], off sc1 nt
	v_lshl_add_u64 v[142:143], v[142:143], 0, s[20:21]
	global_load_dwordx4 v[142:145], v[142:143], off sc1 nt
	s_add_u32 s50, s12, s10
	s_waitcnt vmcnt(6)
	s_addc_u32 s51, s13, 0
	s_mov_b32 m0, s36
	s_waitcnt lgkmcnt(0)
	s_barrier
	v_lshl_add_u64 v[170:171], s[50:51], 0, v[146:147]
	global_load_lds_dwordx4 v[170:171], off
	v_lshl_add_u64 v[170:171], s[50:51], 0, v[156:157]
	s_add_i32 m0, s36, 0x2000
	s_add_i32 s35, s35, 64
	global_load_lds_dwordx4 v[170:171], off
	s_cmp_gt_u32 s37, 13
	s_mov_b32 s36, s37
	s_cbranch_scc0 .Lmoe_G3_1091
